# P5 GLA combine loop rewritten: 16 items per group (48 loads in flight), 64-lane sum of squares reduced with v_permlane32/16_swap + DPP row rotations instead of six ds_bpermute round trips per item; pa
# baseline (speedup 1.0000x reference)
.LBB0_626:
	s_cmp_lt_i32 s90, 6
	s_cselect_b64 s[2:3], -1, 0
	s_and_b64 s[2:3], s[2:3], s[0:1]
	s_andn2_b64 vcc, exec, s[2:3]
	s_cbranch_vccnz .LBB0_653
	s_waitcnt lgkmcnt(0)
	s_add_u32 s20, s88, 0x1ea00000
	s_addc_u32 s21, s89, 0
	s_lshl_b32 s6, s94, 3
	s_add_i32 s10, s79, s6
	s_cmp_gt_i32 s10, 0xffff
	s_cbranch_scc1 .LBB0_636
	s_waitcnt vmcnt(0)
	v_lshlrev_b32_e32 v6, 3, v196
	v_lshlrev_b32_e32 v1, 4, v196
	global_load_dwordx4 v[2:5], v1, s[38:39]
	v_mov_b32_e32 v7, 0x358637bd
	s_lshl_b32 s9, s92, 3
	s_lshl_b32 s11, s92, 7
	s_add_u32 s0, s88, 0x37800000
	s_addc_u32 s1, s89, 0
	s_add_u32 s4, s88, 0x3b800000
	s_addc_u32 s5, s89, 0
	s_add_u32 s22, s20, 0x1000
	s_addc_u32 s23, s21, 0
	s_add_u32 s24, s88, 0x2bf00000
	s_addc_u32 s25, s89, 0
	s_mov_b32 s14, s10
	s_min_i32 s15, s14, 0xffff
	s_lshl_b32 s16, s15, 9
	s_lshr_b32 s17, s15, 2
	s_and_b32 s18, s15, 3
	s_mul_i32 s17, s17, 0x3200
	s_lshl_b32 s18, s18, 9
	s_add_i32 s17, s17, s18
	v_add_u32_e32 v224, s16, v6
	v_add_u32_e32 v225, s17, v6
	global_load_dwordx2 v[8:9], v224, s[0:1]
	global_load_dwordx2 v[10:11], v224, s[4:5]
	global_load_dwordx2 v[12:13], v225, s[22:23]
	s_add_i32 s14, s14, s9
	s_min_i32 s15, s14, 0xffff
	s_lshl_b32 s16, s15, 9
	s_lshr_b32 s17, s15, 2
	s_and_b32 s18, s15, 3
	s_mul_i32 s17, s17, 0x3200
	s_lshl_b32 s18, s18, 9
	s_add_i32 s17, s17, s18
	v_add_u32_e32 v226, s16, v6
	v_add_u32_e32 v227, s17, v6
	global_load_dwordx2 v[14:15], v226, s[0:1]
	global_load_dwordx2 v[16:17], v226, s[4:5]
	global_load_dwordx2 v[18:19], v227, s[22:23]
	s_add_i32 s14, s14, s9
	s_min_i32 s15, s14, 0xffff
	s_lshl_b32 s16, s15, 9
	s_lshr_b32 s17, s15, 2
	s_and_b32 s18, s15, 3
	s_mul_i32 s17, s17, 0x3200
	s_lshl_b32 s18, s18, 9
	s_add_i32 s17, s17, s18
	v_add_u32_e32 v224, s16, v6
	v_add_u32_e32 v225, s17, v6
	global_load_dwordx2 v[20:21], v224, s[0:1]
	global_load_dwordx2 v[22:23], v224, s[4:5]
	global_load_dwordx2 v[24:25], v225, s[22:23]
	s_add_i32 s14, s14, s9
	s_min_i32 s15, s14, 0xffff
	s_lshl_b32 s16, s15, 9
	s_lshr_b32 s17, s15, 2
	s_and_b32 s18, s15, 3
	s_mul_i32 s17, s17, 0x3200
	s_lshl_b32 s18, s18, 9
	s_add_i32 s17, s17, s18
	v_add_u32_e32 v226, s16, v6
	v_add_u32_e32 v227, s17, v6
	global_load_dwordx2 v[26:27], v226, s[0:1]
	global_load_dwordx2 v[28:29], v226, s[4:5]
	global_load_dwordx2 v[30:31], v227, s[22:23]
	s_add_i32 s14, s14, s9
	s_min_i32 s15, s14, 0xffff
	s_lshl_b32 s16, s15, 9
	s_lshr_b32 s17, s15, 2
	s_and_b32 s18, s15, 3
	s_mul_i32 s17, s17, 0x3200
	s_lshl_b32 s18, s18, 9
	s_add_i32 s17, s17, s18
	v_add_u32_e32 v224, s16, v6
	v_add_u32_e32 v225, s17, v6
	global_load_dwordx2 v[32:33], v224, s[0:1]
	global_load_dwordx2 v[34:35], v224, s[4:5]
	global_load_dwordx2 v[36:37], v225, s[22:23]
	s_add_i32 s14, s14, s9
	s_min_i32 s15, s14, 0xffff
	s_lshl_b32 s16, s15, 9
	s_lshr_b32 s17, s15, 2
	s_and_b32 s18, s15, 3
	s_mul_i32 s17, s17, 0x3200
	s_lshl_b32 s18, s18, 9
	s_add_i32 s17, s17, s18
	v_add_u32_e32 v226, s16, v6
	v_add_u32_e32 v227, s17, v6
	global_load_dwordx2 v[38:39], v226, s[0:1]
	global_load_dwordx2 v[40:41], v226, s[4:5]
	global_load_dwordx2 v[42:43], v227, s[22:23]
	s_add_i32 s14, s14, s9
	s_min_i32 s15, s14, 0xffff
	s_lshl_b32 s16, s15, 9
	s_lshr_b32 s17, s15, 2
	s_and_b32 s18, s15, 3
	s_mul_i32 s17, s17, 0x3200
	s_lshl_b32 s18, s18, 9
	s_add_i32 s17, s17, s18
	v_add_u32_e32 v224, s16, v6
	v_add_u32_e32 v225, s17, v6
	global_load_dwordx2 v[44:45], v224, s[0:1]
	global_load_dwordx2 v[46:47], v224, s[4:5]
	global_load_dwordx2 v[48:49], v225, s[22:23]
	s_add_i32 s14, s14, s9
	s_min_i32 s15, s14, 0xffff
	s_lshl_b32 s16, s15, 9
	s_lshr_b32 s17, s15, 2
	s_and_b32 s18, s15, 3
	s_mul_i32 s17, s17, 0x3200
	s_lshl_b32 s18, s18, 9
	s_add_i32 s17, s17, s18
	v_add_u32_e32 v226, s16, v6
	v_add_u32_e32 v227, s17, v6
	global_load_dwordx2 v[50:51], v226, s[0:1]
	global_load_dwordx2 v[52:53], v226, s[4:5]
	global_load_dwordx2 v[54:55], v227, s[22:23]
	s_add_i32 s14, s14, s9
	s_min_i32 s15, s14, 0xffff
	s_lshl_b32 s16, s15, 9
	s_lshr_b32 s17, s15, 2
	s_and_b32 s18, s15, 3
	s_mul_i32 s17, s17, 0x3200
	s_lshl_b32 s18, s18, 9
	s_add_i32 s17, s17, s18
	v_add_u32_e32 v224, s16, v6
	v_add_u32_e32 v225, s17, v6
	global_load_dwordx2 v[56:57], v224, s[0:1]
	global_load_dwordx2 v[58:59], v224, s[4:5]
	global_load_dwordx2 v[60:61], v225, s[22:23]
	s_add_i32 s14, s14, s9
	s_min_i32 s15, s14, 0xffff
	s_lshl_b32 s16, s15, 9
	s_lshr_b32 s17, s15, 2
	s_and_b32 s18, s15, 3
	s_mul_i32 s17, s17, 0x3200
	s_lshl_b32 s18, s18, 9
	s_add_i32 s17, s17, s18
	v_add_u32_e32 v226, s16, v6
	v_add_u32_e32 v227, s17, v6
	global_load_dwordx2 v[62:63], v226, s[0:1]
	global_load_dwordx2 v[64:65], v226, s[4:5]
	global_load_dwordx2 v[66:67], v227, s[22:23]
	s_add_i32 s14, s14, s9
	s_min_i32 s15, s14, 0xffff
	s_lshl_b32 s16, s15, 9
	s_lshr_b32 s17, s15, 2
	s_and_b32 s18, s15, 3
	s_mul_i32 s17, s17, 0x3200
	s_lshl_b32 s18, s18, 9
	s_add_i32 s17, s17, s18
	v_add_u32_e32 v224, s16, v6
	v_add_u32_e32 v225, s17, v6
	global_load_dwordx2 v[68:69], v224, s[0:1]
	global_load_dwordx2 v[70:71], v224, s[4:5]
	global_load_dwordx2 v[72:73], v225, s[22:23]
	s_add_i32 s14, s14, s9
	s_min_i32 s15, s14, 0xffff
	s_lshl_b32 s16, s15, 9
	s_lshr_b32 s17, s15, 2
	s_and_b32 s18, s15, 3
	s_mul_i32 s17, s17, 0x3200
	s_lshl_b32 s18, s18, 9
	s_add_i32 s17, s17, s18
	v_add_u32_e32 v226, s16, v6
	v_add_u32_e32 v227, s17, v6
	global_load_dwordx2 v[74:75], v226, s[0:1]
	global_load_dwordx2 v[76:77], v226, s[4:5]
	global_load_dwordx2 v[78:79], v227, s[22:23]
	s_add_i32 s14, s14, s9
	s_min_i32 s15, s14, 0xffff
	s_lshl_b32 s16, s15, 9
	s_lshr_b32 s17, s15, 2
	s_and_b32 s18, s15, 3
	s_mul_i32 s17, s17, 0x3200
	s_lshl_b32 s18, s18, 9
	s_add_i32 s17, s17, s18
	v_add_u32_e32 v224, s16, v6
	v_add_u32_e32 v225, s17, v6
	global_load_dwordx2 v[80:81], v224, s[0:1]
	global_load_dwordx2 v[82:83], v224, s[4:5]
	global_load_dwordx2 v[84:85], v225, s[22:23]
	s_add_i32 s14, s14, s9
	s_min_i32 s15, s14, 0xffff
	s_lshl_b32 s16, s15, 9
	s_lshr_b32 s17, s15, 2
	s_and_b32 s18, s15, 3
	s_mul_i32 s17, s17, 0x3200
	s_lshl_b32 s18, s18, 9
	s_add_i32 s17, s17, s18
	v_add_u32_e32 v226, s16, v6
	v_add_u32_e32 v227, s17, v6
	global_load_dwordx2 v[86:87], v226, s[0:1]
	global_load_dwordx2 v[88:89], v226, s[4:5]
	global_load_dwordx2 v[90:91], v227, s[22:23]
	s_add_i32 s14, s14, s9
	s_min_i32 s15, s14, 0xffff
	s_lshl_b32 s16, s15, 9
	s_lshr_b32 s17, s15, 2
	s_and_b32 s18, s15, 3
	s_mul_i32 s17, s17, 0x3200
	s_lshl_b32 s18, s18, 9
	s_add_i32 s17, s17, s18
	v_add_u32_e32 v224, s16, v6
	v_add_u32_e32 v225, s17, v6
	global_load_dwordx2 v[92:93], v224, s[0:1]
	global_load_dwordx2 v[94:95], v224, s[4:5]
	global_load_dwordx2 v[96:97], v225, s[22:23]
	s_add_i32 s14, s14, s9
	s_min_i32 s15, s14, 0xffff
	s_lshl_b32 s16, s15, 9
	s_lshr_b32 s17, s15, 2
	s_and_b32 s18, s15, 3
	s_mul_i32 s17, s17, 0x3200
	s_lshl_b32 s18, s18, 9
	s_add_i32 s17, s17, s18
	v_add_u32_e32 v226, s16, v6
	v_add_u32_e32 v227, s17, v6
	global_load_dwordx2 v[98:99], v226, s[0:1]
	global_load_dwordx2 v[100:101], v226, s[4:5]
	global_load_dwordx2 v[102:103], v227, s[22:23]
.Lgc_loop:
	s_add_i32 s19, s10, s11
	s_mov_b32 s14, s19
	s_min_i32 s15, s14, 0xffff
	s_lshl_b32 s16, s15, 9
	s_lshr_b32 s17, s15, 2
	s_and_b32 s18, s15, 3
	s_mul_i32 s17, s17, 0x3200
	s_lshl_b32 s18, s18, 9
	s_add_i32 s17, s17, s18
	v_add_u32_e32 v224, s16, v6
	v_add_u32_e32 v225, s17, v6
	global_load_dwordx2 v[104:105], v224, s[0:1]
	global_load_dwordx2 v[106:107], v224, s[4:5]
	global_load_dwordx2 v[108:109], v225, s[22:23]
	s_add_i32 s14, s14, s9
	s_min_i32 s15, s14, 0xffff
	s_lshl_b32 s16, s15, 9
	s_lshr_b32 s17, s15, 2
	s_and_b32 s18, s15, 3
	s_mul_i32 s17, s17, 0x3200
	s_lshl_b32 s18, s18, 9
	s_add_i32 s17, s17, s18
	v_add_u32_e32 v226, s16, v6
	v_add_u32_e32 v227, s17, v6
	global_load_dwordx2 v[110:111], v226, s[0:1]
	global_load_dwordx2 v[112:113], v226, s[4:5]
	global_load_dwordx2 v[114:115], v227, s[22:23]
	s_add_i32 s14, s14, s9
	s_min_i32 s15, s14, 0xffff
	s_lshl_b32 s16, s15, 9
	s_lshr_b32 s17, s15, 2
	s_and_b32 s18, s15, 3
	s_mul_i32 s17, s17, 0x3200
	s_lshl_b32 s18, s18, 9
	s_add_i32 s17, s17, s18
	v_add_u32_e32 v224, s16, v6
	v_add_u32_e32 v225, s17, v6
	global_load_dwordx2 v[116:117], v224, s[0:1]
	global_load_dwordx2 v[118:119], v224, s[4:5]
	global_load_dwordx2 v[120:121], v225, s[22:23]
	s_add_i32 s14, s14, s9
	s_min_i32 s15, s14, 0xffff
	s_lshl_b32 s16, s15, 9
	s_lshr_b32 s17, s15, 2
	s_and_b32 s18, s15, 3
	s_mul_i32 s17, s17, 0x3200
	s_lshl_b32 s18, s18, 9
	s_add_i32 s17, s17, s18
	v_add_u32_e32 v226, s16, v6
	v_add_u32_e32 v227, s17, v6
	global_load_dwordx2 v[122:123], v226, s[0:1]
	global_load_dwordx2 v[124:125], v226, s[4:5]
	global_load_dwordx2 v[126:127], v227, s[22:23]
	s_add_i32 s14, s14, s9
	s_min_i32 s15, s14, 0xffff
	s_lshl_b32 s16, s15, 9
	s_lshr_b32 s17, s15, 2
	s_and_b32 s18, s15, 3
	s_mul_i32 s17, s17, 0x3200
	s_lshl_b32 s18, s18, 9
	s_add_i32 s17, s17, s18
	v_add_u32_e32 v224, s16, v6
	v_add_u32_e32 v225, s17, v6
	global_load_dwordx2 v[128:129], v224, s[0:1]
	global_load_dwordx2 v[130:131], v224, s[4:5]
	global_load_dwordx2 v[132:133], v225, s[22:23]
	s_add_i32 s14, s14, s9
	s_min_i32 s15, s14, 0xffff
	s_lshl_b32 s16, s15, 9
	s_lshr_b32 s17, s15, 2
	s_and_b32 s18, s15, 3
	s_mul_i32 s17, s17, 0x3200
	s_lshl_b32 s18, s18, 9
	s_add_i32 s17, s17, s18
	v_add_u32_e32 v226, s16, v6
	v_add_u32_e32 v227, s17, v6
	global_load_dwordx2 v[134:135], v226, s[0:1]
	global_load_dwordx2 v[136:137], v226, s[4:5]
	global_load_dwordx2 v[138:139], v227, s[22:23]
	s_add_i32 s14, s14, s9
	s_min_i32 s15, s14, 0xffff
	s_lshl_b32 s16, s15, 9
	s_lshr_b32 s17, s15, 2
	s_and_b32 s18, s15, 3
	s_mul_i32 s17, s17, 0x3200
	s_lshl_b32 s18, s18, 9
	s_add_i32 s17, s17, s18
	v_add_u32_e32 v224, s16, v6
	v_add_u32_e32 v225, s17, v6
	global_load_dwordx2 v[140:141], v224, s[0:1]
	global_load_dwordx2 v[142:143], v224, s[4:5]
	global_load_dwordx2 v[144:145], v225, s[22:23]
	s_add_i32 s14, s14, s9
	s_min_i32 s15, s14, 0xffff
	s_lshl_b32 s16, s15, 9
	s_lshr_b32 s17, s15, 2
	s_and_b32 s18, s15, 3
	s_mul_i32 s17, s17, 0x3200
	s_lshl_b32 s18, s18, 9
	s_add_i32 s17, s17, s18
	v_add_u32_e32 v226, s16, v6
	v_add_u32_e32 v227, s17, v6
	global_load_dwordx2 v[146:147], v226, s[0:1]
	global_load_dwordx2 v[148:149], v226, s[4:5]
	global_load_dwordx2 v[150:151], v227, s[22:23]
	s_add_i32 s14, s14, s9
	s_min_i32 s15, s14, 0xffff
	s_lshl_b32 s16, s15, 9
	s_lshr_b32 s17, s15, 2
	s_and_b32 s18, s15, 3
	s_mul_i32 s17, s17, 0x3200
	s_lshl_b32 s18, s18, 9
	s_add_i32 s17, s17, s18
	v_add_u32_e32 v224, s16, v6
	v_add_u32_e32 v225, s17, v6
	global_load_dwordx2 v[152:153], v224, s[0:1]
	global_load_dwordx2 v[154:155], v224, s[4:5]
	global_load_dwordx2 v[156:157], v225, s[22:23]
	s_add_i32 s14, s14, s9
	s_min_i32 s15, s14, 0xffff
	s_lshl_b32 s16, s15, 9
	s_lshr_b32 s17, s15, 2
	s_and_b32 s18, s15, 3
	s_mul_i32 s17, s17, 0x3200
	s_lshl_b32 s18, s18, 9
	s_add_i32 s17, s17, s18
	v_add_u32_e32 v226, s16, v6
	v_add_u32_e32 v227, s17, v6
	global_load_dwordx2 v[158:159], v226, s[0:1]
	global_load_dwordx2 v[160:161], v226, s[4:5]
	global_load_dwordx2 v[162:163], v227, s[22:23]
	s_add_i32 s14, s14, s9
	s_min_i32 s15, s14, 0xffff
	s_lshl_b32 s16, s15, 9
	s_lshr_b32 s17, s15, 2
	s_and_b32 s18, s15, 3
	s_mul_i32 s17, s17, 0x3200
	s_lshl_b32 s18, s18, 9
	s_add_i32 s17, s17, s18
	v_add_u32_e32 v224, s16, v6
	v_add_u32_e32 v225, s17, v6
	global_load_dwordx2 v[164:165], v224, s[0:1]
	global_load_dwordx2 v[166:167], v224, s[4:5]
	global_load_dwordx2 v[168:169], v225, s[22:23]
	s_add_i32 s14, s14, s9
	s_min_i32 s15, s14, 0xffff
	s_lshl_b32 s16, s15, 9
	s_lshr_b32 s17, s15, 2
	s_and_b32 s18, s15, 3
	s_mul_i32 s17, s17, 0x3200
	s_lshl_b32 s18, s18, 9
	s_add_i32 s17, s17, s18
	v_add_u32_e32 v226, s16, v6
	v_add_u32_e32 v227, s17, v6
	global_load_dwordx2 v[170:171], v226, s[0:1]
	global_load_dwordx2 v[172:173], v226, s[4:5]
	global_load_dwordx2 v[174:175], v227, s[22:23]
	s_add_i32 s14, s14, s9
	s_min_i32 s15, s14, 0xffff
	s_lshl_b32 s16, s15, 9
	s_lshr_b32 s17, s15, 2
	s_and_b32 s18, s15, 3
	s_mul_i32 s17, s17, 0x3200
	s_lshl_b32 s18, s18, 9
	s_add_i32 s17, s17, s18
	v_add_u32_e32 v224, s16, v6
	v_add_u32_e32 v225, s17, v6
	global_load_dwordx2 v[176:177], v224, s[0:1]
	global_load_dwordx2 v[178:179], v224, s[4:5]
	global_load_dwordx2 v[180:181], v225, s[22:23]
	s_add_i32 s14, s14, s9
	s_min_i32 s15, s14, 0xffff
	s_lshl_b32 s16, s15, 9
	s_lshr_b32 s17, s15, 2
	s_and_b32 s18, s15, 3
	s_mul_i32 s17, s17, 0x3200
	s_lshl_b32 s18, s18, 9
	s_add_i32 s17, s17, s18
	v_add_u32_e32 v226, s16, v6
	v_add_u32_e32 v227, s17, v6
	global_load_dwordx2 v[182:183], v226, s[0:1]
	global_load_dwordx2 v[184:185], v226, s[4:5]
	global_load_dwordx2 v[186:187], v227, s[22:23]
	s_add_i32 s14, s14, s9
	s_min_i32 s15, s14, 0xffff
	s_lshl_b32 s16, s15, 9
	s_lshr_b32 s17, s15, 2
	s_and_b32 s18, s15, 3
	s_mul_i32 s17, s17, 0x3200
	s_lshl_b32 s18, s18, 9
	s_add_i32 s17, s17, s18
	v_add_u32_e32 v224, s16, v6
	v_add_u32_e32 v225, s17, v6
	global_load_dwordx2 v[188:189], v224, s[0:1]
	global_load_dwordx2 v[190:191], v224, s[4:5]
	global_load_dwordx2 v[192:193], v225, s[22:23]
	s_add_i32 s14, s14, s9
	s_min_i32 s15, s14, 0xffff
	s_lshl_b32 s16, s15, 9
	s_lshr_b32 s17, s15, 2
	s_and_b32 s18, s15, 3
	s_mul_i32 s17, s17, 0x3200
	s_lshl_b32 s18, s18, 9
	s_add_i32 s17, s17, s18
	v_add_u32_e32 v226, s16, v6
	v_add_u32_e32 v227, s17, v6
	global_load_dwordx2 v[198:199], v226, s[0:1]
	global_load_dwordx2 v[200:201], v226, s[4:5]
	global_load_dwordx2 v[202:203], v227, s[22:23]
	s_waitcnt vmcnt(48)
	s_mov_b32 s14, s10
	v_lshlrev_b32_e32 v204, 16, v8
	v_lshlrev_b32_e32 v224, 16, v10
	v_and_b32_e32 v205, 0xffff0000, v8
	v_and_b32_e32 v225, 0xffff0000, v10
	v_add_f32_e32 v204, v204, v224
	v_add_f32_e32 v205, v205, v225
	v_lshlrev_b32_e32 v206, 16, v9
	v_lshlrev_b32_e32 v224, 16, v11
	v_and_b32_e32 v207, 0xffff0000, v9
	v_and_b32_e32 v225, 0xffff0000, v11
	v_add_f32_e32 v206, v206, v224
	v_add_f32_e32 v207, v207, v225
	v_mul_f32_e32 v224, v204, v204
	v_mul_f32_e32 v225, v205, v205
	v_add_f32_e32 v220, v224, v225
	v_mul_f32_e32 v224, v206, v206
	v_mul_f32_e32 v225, v207, v207
	v_add_f32_e32 v220, v224, v220
	v_add_f32_e32 v220, v225, v220
	v_lshlrev_b32_e32 v208, 16, v14
	v_lshlrev_b32_e32 v226, 16, v16
	v_and_b32_e32 v209, 0xffff0000, v14
	v_and_b32_e32 v227, 0xffff0000, v16
	v_add_f32_e32 v208, v208, v226
	v_add_f32_e32 v209, v209, v227
	v_lshlrev_b32_e32 v210, 16, v15
	v_lshlrev_b32_e32 v226, 16, v17
	v_and_b32_e32 v211, 0xffff0000, v15
	v_and_b32_e32 v227, 0xffff0000, v17
	v_add_f32_e32 v210, v210, v226
	v_add_f32_e32 v211, v211, v227
	v_mul_f32_e32 v226, v208, v208
	v_mul_f32_e32 v227, v209, v209
	v_add_f32_e32 v221, v226, v227
	v_mul_f32_e32 v226, v210, v210
	v_mul_f32_e32 v227, v211, v211
	v_add_f32_e32 v221, v226, v221
	v_add_f32_e32 v221, v227, v221
	v_lshlrev_b32_e32 v212, 16, v20
	v_lshlrev_b32_e32 v224, 16, v22
	v_and_b32_e32 v213, 0xffff0000, v20
	v_and_b32_e32 v225, 0xffff0000, v22
	v_add_f32_e32 v212, v212, v224
	v_add_f32_e32 v213, v213, v225
	v_lshlrev_b32_e32 v214, 16, v21
	v_lshlrev_b32_e32 v224, 16, v23
	v_and_b32_e32 v215, 0xffff0000, v21
	v_and_b32_e32 v225, 0xffff0000, v23
	v_add_f32_e32 v214, v214, v224
	v_add_f32_e32 v215, v215, v225
	v_mul_f32_e32 v224, v212, v212
	v_mul_f32_e32 v225, v213, v213
	v_add_f32_e32 v222, v224, v225
	v_mul_f32_e32 v224, v214, v214
	v_mul_f32_e32 v225, v215, v215
	v_add_f32_e32 v222, v224, v222
	v_add_f32_e32 v222, v225, v222
	v_lshlrev_b32_e32 v216, 16, v26
	v_lshlrev_b32_e32 v226, 16, v28
	v_and_b32_e32 v217, 0xffff0000, v26
	v_and_b32_e32 v227, 0xffff0000, v28
	v_add_f32_e32 v216, v216, v226
	v_add_f32_e32 v217, v217, v227
	v_lshlrev_b32_e32 v218, 16, v27
	v_lshlrev_b32_e32 v226, 16, v29
	v_and_b32_e32 v219, 0xffff0000, v27
	v_and_b32_e32 v227, 0xffff0000, v29
	v_add_f32_e32 v218, v218, v226
	v_add_f32_e32 v219, v219, v227
	v_mul_f32_e32 v226, v216, v216
	v_mul_f32_e32 v227, v217, v217
	v_add_f32_e32 v223, v226, v227
	v_mul_f32_e32 v226, v218, v218
	v_mul_f32_e32 v227, v219, v219
	v_add_f32_e32 v223, v226, v223
	v_add_f32_e32 v223, v227, v223
	v_mov_b32_e32 v224, v220
	v_mov_b32_e32 v225, v221
	v_mov_b32_e32 v226, v222
	v_mov_b32_e32 v227, v223
	v_permlane32_swap_b32_e32 v220, v224
	v_permlane32_swap_b32_e32 v221, v225
	v_permlane32_swap_b32_e32 v222, v226
	v_permlane32_swap_b32_e32 v223, v227
	v_add_f32_e32 v220, v220, v224
	v_add_f32_e32 v221, v221, v225
	v_add_f32_e32 v222, v222, v226
	v_add_f32_e32 v223, v223, v227
	v_mov_b32_e32 v224, v220
	v_mov_b32_e32 v225, v221
	v_mov_b32_e32 v226, v222
	v_mov_b32_e32 v227, v223
	v_permlane16_swap_b32_e32 v220, v224
	v_permlane16_swap_b32_e32 v221, v225
	v_permlane16_swap_b32_e32 v222, v226
	v_permlane16_swap_b32_e32 v223, v227
	v_add_f32_e32 v220, v220, v224
	v_add_f32_e32 v221, v221, v225
	v_add_f32_e32 v222, v222, v226
	v_add_f32_e32 v223, v223, v227
	v_add_f32_dpp v220, v220, v220 row_ror:8 row_mask:0xf bank_mask:0xf
	v_add_f32_dpp v221, v221, v221 row_ror:8 row_mask:0xf bank_mask:0xf
	v_add_f32_dpp v222, v222, v222 row_ror:8 row_mask:0xf bank_mask:0xf
	v_add_f32_dpp v223, v223, v223 row_ror:8 row_mask:0xf bank_mask:0xf
	v_add_f32_dpp v220, v220, v220 row_ror:4 row_mask:0xf bank_mask:0xf
	v_add_f32_dpp v221, v221, v221 row_ror:4 row_mask:0xf bank_mask:0xf
	v_add_f32_dpp v222, v222, v222 row_ror:4 row_mask:0xf bank_mask:0xf
	v_add_f32_dpp v223, v223, v223 row_ror:4 row_mask:0xf bank_mask:0xf
	v_add_f32_dpp v220, v220, v220 row_ror:2 row_mask:0xf bank_mask:0xf
	v_add_f32_dpp v221, v221, v221 row_ror:2 row_mask:0xf bank_mask:0xf
	v_add_f32_dpp v222, v222, v222 row_ror:2 row_mask:0xf bank_mask:0xf
	v_add_f32_dpp v223, v223, v223 row_ror:2 row_mask:0xf bank_mask:0xf
	v_add_f32_dpp v220, v220, v220 row_ror:1 row_mask:0xf bank_mask:0xf
	v_add_f32_dpp v221, v221, v221 row_ror:1 row_mask:0xf bank_mask:0xf
	v_add_f32_dpp v222, v222, v222 row_ror:1 row_mask:0xf bank_mask:0xf
	v_add_f32_dpp v223, v223, v223 row_ror:1 row_mask:0xf bank_mask:0xf
	v_fmamk_f32 v226, v220, 0x3b800000, v7
	v_rsq_f32_e32 v226, v226
	v_lshlrev_b32_e32 v224, 16, v12
	v_lshlrev_b32_e32 v225, 16, v13
	v_mul_f32_e32 v204, v204, v226
	v_mul_f32_e32 v205, v205, v226
	v_mul_f32_e32 v206, v206, v226
	v_mul_f32_e32 v207, v207, v226
	v_mul_f32_e32 v204, v2, v204
	v_mul_f32_e32 v205, v3, v205
	v_mul_f32_e32 v206, v4, v206
	v_mul_f32_e32 v207, v5, v207
	v_and_b32_e32 v12, 0xffff0000, v12
	v_and_b32_e32 v13, 0xffff0000, v13
	v_mul_f32_e32 v226, 0xbfb8aa3b, v224
	v_mul_f32_e32 v227, 0xbfb8aa3b, v12
	v_mul_f32_e32 v1, 0xbfb8aa3b, v225
	v_mul_f32_e32 v220, 0xbfb8aa3b, v13
	v_exp_f32_e32 v226, v226
	v_exp_f32_e32 v227, v227
	v_exp_f32_e32 v1, v1
	v_exp_f32_e32 v220, v220
	v_add_f32_e32 v226, 1.0, v226
	v_add_f32_e32 v227, 1.0, v227
	v_add_f32_e32 v1, 1.0, v1
	v_add_f32_e32 v220, 1.0, v220
	v_rcp_f32_e32 v226, v226
	v_rcp_f32_e32 v227, v227
	v_rcp_f32_e32 v1, v1
	v_rcp_f32_e32 v220, v220
	v_mul_f32_e32 v224, v226, v224
	v_mul_f32_e32 v12, v227, v12
	v_mul_f32_e32 v225, v1, v225
	v_mul_f32_e32 v13, v220, v13
	v_mul_f32_e32 v204, v224, v204
	v_mul_f32_e32 v205, v12, v205
	v_mul_f32_e32 v206, v225, v206
	v_mul_f32_e32 v207, v13, v207
	v_cvt_pk_bf16_f32 v224, v204, v205
	v_cvt_pk_bf16_f32 v225, v206, v207
	s_cmp_gt_i32 s14, 0xffff
	s_cbranch_scc1 .Lgc_skip_a_0
	s_lshr_b32 s17, s14, 2
	s_and_b32 s18, s14, 3
	s_lshl_b32 s17, s17, 12
	s_lshl_b32 s18, s18, 9
	s_add_i32 s17, s17, s18
	v_add_u32_e32 v227, s17, v6
	global_store_dwordx2 v227, v[224:225], s[24:25]
.Lgc_skip_a_0:
	s_add_i32 s14, s14, s9
	v_fmamk_f32 v224, v221, 0x3b800000, v7
	v_rsq_f32_e32 v224, v224
	v_lshlrev_b32_e32 v226, 16, v18
	v_lshlrev_b32_e32 v227, 16, v19
	v_mul_f32_e32 v208, v208, v224
	v_mul_f32_e32 v209, v209, v224
	v_mul_f32_e32 v210, v210, v224
	v_mul_f32_e32 v211, v211, v224
	v_mul_f32_e32 v208, v2, v208
	v_mul_f32_e32 v209, v3, v209
	v_mul_f32_e32 v210, v4, v210
	v_mul_f32_e32 v211, v5, v211
	v_and_b32_e32 v18, 0xffff0000, v18
	v_and_b32_e32 v19, 0xffff0000, v19
	v_mul_f32_e32 v224, 0xbfb8aa3b, v226
	v_mul_f32_e32 v225, 0xbfb8aa3b, v18
	v_mul_f32_e32 v1, 0xbfb8aa3b, v227
	v_mul_f32_e32 v221, 0xbfb8aa3b, v19
	v_exp_f32_e32 v224, v224
	v_exp_f32_e32 v225, v225
	v_exp_f32_e32 v1, v1
	v_exp_f32_e32 v221, v221
	v_add_f32_e32 v224, 1.0, v224
	v_add_f32_e32 v225, 1.0, v225
	v_add_f32_e32 v1, 1.0, v1
	v_add_f32_e32 v221, 1.0, v221
	v_rcp_f32_e32 v224, v224
	v_rcp_f32_e32 v225, v225
	v_rcp_f32_e32 v1, v1
	v_rcp_f32_e32 v221, v221
	v_mul_f32_e32 v226, v224, v226
	v_mul_f32_e32 v18, v225, v18
	v_mul_f32_e32 v227, v1, v227
	v_mul_f32_e32 v19, v221, v19
	v_mul_f32_e32 v208, v226, v208
	v_mul_f32_e32 v209, v18, v209
	v_mul_f32_e32 v210, v227, v210
	v_mul_f32_e32 v211, v19, v211
	v_cvt_pk_bf16_f32 v226, v208, v209
	v_cvt_pk_bf16_f32 v227, v210, v211
	s_cmp_gt_i32 s14, 0xffff
	s_cbranch_scc1 .Lgc_skip_a_1
	s_lshr_b32 s17, s14, 2
	s_and_b32 s18, s14, 3
	s_lshl_b32 s17, s17, 12
	s_lshl_b32 s18, s18, 9
	s_add_i32 s17, s17, s18
	v_add_u32_e32 v225, s17, v6
	global_store_dwordx2 v225, v[226:227], s[24:25]
.Lgc_skip_a_1:
	s_add_i32 s14, s14, s9
	v_fmamk_f32 v226, v222, 0x3b800000, v7
	v_rsq_f32_e32 v226, v226
	v_lshlrev_b32_e32 v224, 16, v24
	v_lshlrev_b32_e32 v225, 16, v25
	v_mul_f32_e32 v212, v212, v226
	v_mul_f32_e32 v213, v213, v226
	v_mul_f32_e32 v214, v214, v226
	v_mul_f32_e32 v215, v215, v226
	v_mul_f32_e32 v212, v2, v212
	v_mul_f32_e32 v213, v3, v213
	v_mul_f32_e32 v214, v4, v214
	v_mul_f32_e32 v215, v5, v215
	v_and_b32_e32 v24, 0xffff0000, v24
	v_and_b32_e32 v25, 0xffff0000, v25
	v_mul_f32_e32 v226, 0xbfb8aa3b, v224
	v_mul_f32_e32 v227, 0xbfb8aa3b, v24
	v_mul_f32_e32 v1, 0xbfb8aa3b, v225
	v_mul_f32_e32 v222, 0xbfb8aa3b, v25
	v_exp_f32_e32 v226, v226
	v_exp_f32_e32 v227, v227
	v_exp_f32_e32 v1, v1
	v_exp_f32_e32 v222, v222
	v_add_f32_e32 v226, 1.0, v226
	v_add_f32_e32 v227, 1.0, v227
	v_add_f32_e32 v1, 1.0, v1
	v_add_f32_e32 v222, 1.0, v222
	v_rcp_f32_e32 v226, v226
	v_rcp_f32_e32 v227, v227
	v_rcp_f32_e32 v1, v1
	v_rcp_f32_e32 v222, v222
	v_mul_f32_e32 v224, v226, v224
	v_mul_f32_e32 v24, v227, v24
	v_mul_f32_e32 v225, v1, v225
	v_mul_f32_e32 v25, v222, v25
	v_mul_f32_e32 v212, v224, v212
	v_mul_f32_e32 v213, v24, v213
	v_mul_f32_e32 v214, v225, v214
	v_mul_f32_e32 v215, v25, v215
	v_cvt_pk_bf16_f32 v224, v212, v213
	v_cvt_pk_bf16_f32 v225, v214, v215
	s_cmp_gt_i32 s14, 0xffff
	s_cbranch_scc1 .Lgc_skip_a_2
	s_lshr_b32 s17, s14, 2
	s_and_b32 s18, s14, 3
	s_lshl_b32 s17, s17, 12
	s_lshl_b32 s18, s18, 9
	s_add_i32 s17, s17, s18
	v_add_u32_e32 v227, s17, v6
	global_store_dwordx2 v227, v[224:225], s[24:25]
.Lgc_skip_a_2:
	s_add_i32 s14, s14, s9
	v_fmamk_f32 v224, v223, 0x3b800000, v7
	v_rsq_f32_e32 v224, v224
	v_lshlrev_b32_e32 v226, 16, v30
	v_lshlrev_b32_e32 v227, 16, v31
	v_mul_f32_e32 v216, v216, v224
	v_mul_f32_e32 v217, v217, v224
	v_mul_f32_e32 v218, v218, v224
	v_mul_f32_e32 v219, v219, v224
	v_mul_f32_e32 v216, v2, v216
	v_mul_f32_e32 v217, v3, v217
	v_mul_f32_e32 v218, v4, v218
	v_mul_f32_e32 v219, v5, v219
	v_and_b32_e32 v30, 0xffff0000, v30
	v_and_b32_e32 v31, 0xffff0000, v31
	v_mul_f32_e32 v224, 0xbfb8aa3b, v226
	v_mul_f32_e32 v225, 0xbfb8aa3b, v30
	v_mul_f32_e32 v1, 0xbfb8aa3b, v227
	v_mul_f32_e32 v223, 0xbfb8aa3b, v31
	v_exp_f32_e32 v224, v224
	v_exp_f32_e32 v225, v225
	v_exp_f32_e32 v1, v1
	v_exp_f32_e32 v223, v223
	v_add_f32_e32 v224, 1.0, v224
	v_add_f32_e32 v225, 1.0, v225
	v_add_f32_e32 v1, 1.0, v1
	v_add_f32_e32 v223, 1.0, v223
	v_rcp_f32_e32 v224, v224
	v_rcp_f32_e32 v225, v225
	v_rcp_f32_e32 v1, v1
	v_rcp_f32_e32 v223, v223
	v_mul_f32_e32 v226, v224, v226
	v_mul_f32_e32 v30, v225, v30
	v_mul_f32_e32 v227, v1, v227
	v_mul_f32_e32 v31, v223, v31
	v_mul_f32_e32 v216, v226, v216
	v_mul_f32_e32 v217, v30, v217
	v_mul_f32_e32 v218, v227, v218
	v_mul_f32_e32 v219, v31, v219
	v_cvt_pk_bf16_f32 v226, v216, v217
	v_cvt_pk_bf16_f32 v227, v218, v219
	s_cmp_gt_i32 s14, 0xffff
	s_cbranch_scc1 .Lgc_skip_a_3
	s_lshr_b32 s17, s14, 2
	s_and_b32 s18, s14, 3
	s_lshl_b32 s17, s17, 12
	s_lshl_b32 s18, s18, 9
	s_add_i32 s17, s17, s18
	v_add_u32_e32 v225, s17, v6
	global_store_dwordx2 v225, v[226:227], s[24:25]
.Lgc_skip_a_3:
	s_add_i32 s14, s14, s9
	v_lshlrev_b32_e32 v204, 16, v32
	v_lshlrev_b32_e32 v224, 16, v34
	v_and_b32_e32 v205, 0xffff0000, v32
	v_and_b32_e32 v225, 0xffff0000, v34
	v_add_f32_e32 v204, v204, v224
	v_add_f32_e32 v205, v205, v225
	v_lshlrev_b32_e32 v206, 16, v33
	v_lshlrev_b32_e32 v224, 16, v35
	v_and_b32_e32 v207, 0xffff0000, v33
	v_and_b32_e32 v225, 0xffff0000, v35
	v_add_f32_e32 v206, v206, v224
	v_add_f32_e32 v207, v207, v225
	v_mul_f32_e32 v224, v204, v204
	v_mul_f32_e32 v225, v205, v205
	v_add_f32_e32 v220, v224, v225
	v_mul_f32_e32 v224, v206, v206
	v_mul_f32_e32 v225, v207, v207
	v_add_f32_e32 v220, v224, v220
	v_add_f32_e32 v220, v225, v220
	v_lshlrev_b32_e32 v208, 16, v38
	v_lshlrev_b32_e32 v226, 16, v40
	v_and_b32_e32 v209, 0xffff0000, v38
	v_and_b32_e32 v227, 0xffff0000, v40
	v_add_f32_e32 v208, v208, v226
	v_add_f32_e32 v209, v209, v227
	v_lshlrev_b32_e32 v210, 16, v39
	v_lshlrev_b32_e32 v226, 16, v41
	v_and_b32_e32 v211, 0xffff0000, v39
	v_and_b32_e32 v227, 0xffff0000, v41
	v_add_f32_e32 v210, v210, v226
	v_add_f32_e32 v211, v211, v227
	v_mul_f32_e32 v226, v208, v208
	v_mul_f32_e32 v227, v209, v209
	v_add_f32_e32 v221, v226, v227
	v_mul_f32_e32 v226, v210, v210
	v_mul_f32_e32 v227, v211, v211
	v_add_f32_e32 v221, v226, v221
	v_add_f32_e32 v221, v227, v221
	v_lshlrev_b32_e32 v212, 16, v44
	v_lshlrev_b32_e32 v224, 16, v46
	v_and_b32_e32 v213, 0xffff0000, v44
	v_and_b32_e32 v225, 0xffff0000, v46
	v_add_f32_e32 v212, v212, v224
	v_add_f32_e32 v213, v213, v225
	v_lshlrev_b32_e32 v214, 16, v45
	v_lshlrev_b32_e32 v224, 16, v47
	v_and_b32_e32 v215, 0xffff0000, v45
	v_and_b32_e32 v225, 0xffff0000, v47
	v_add_f32_e32 v214, v214, v224
	v_add_f32_e32 v215, v215, v225
	v_mul_f32_e32 v224, v212, v212
	v_mul_f32_e32 v225, v213, v213
	v_add_f32_e32 v222, v224, v225
	v_mul_f32_e32 v224, v214, v214
	v_mul_f32_e32 v225, v215, v215
	v_add_f32_e32 v222, v224, v222
	v_add_f32_e32 v222, v225, v222
	v_lshlrev_b32_e32 v216, 16, v50
	v_lshlrev_b32_e32 v226, 16, v52
	v_and_b32_e32 v217, 0xffff0000, v50
	v_and_b32_e32 v227, 0xffff0000, v52
	v_add_f32_e32 v216, v216, v226
	v_add_f32_e32 v217, v217, v227
	v_lshlrev_b32_e32 v218, 16, v51
	v_lshlrev_b32_e32 v226, 16, v53
	v_and_b32_e32 v219, 0xffff0000, v51
	v_and_b32_e32 v227, 0xffff0000, v53
	v_add_f32_e32 v218, v218, v226
	v_add_f32_e32 v219, v219, v227
	v_mul_f32_e32 v226, v216, v216
	v_mul_f32_e32 v227, v217, v217
	v_add_f32_e32 v223, v226, v227
	v_mul_f32_e32 v226, v218, v218
	v_mul_f32_e32 v227, v219, v219
	v_add_f32_e32 v223, v226, v223
	v_add_f32_e32 v223, v227, v223
	v_mov_b32_e32 v224, v220
	v_mov_b32_e32 v225, v221
	v_mov_b32_e32 v226, v222
	v_mov_b32_e32 v227, v223
	v_permlane32_swap_b32_e32 v220, v224
	v_permlane32_swap_b32_e32 v221, v225
	v_permlane32_swap_b32_e32 v222, v226
	v_permlane32_swap_b32_e32 v223, v227
	v_add_f32_e32 v220, v220, v224
	v_add_f32_e32 v221, v221, v225
	v_add_f32_e32 v222, v222, v226
	v_add_f32_e32 v223, v223, v227
	v_mov_b32_e32 v224, v220
	v_mov_b32_e32 v225, v221
	v_mov_b32_e32 v226, v222
	v_mov_b32_e32 v227, v223
	v_permlane16_swap_b32_e32 v220, v224
	v_permlane16_swap_b32_e32 v221, v225
	v_permlane16_swap_b32_e32 v222, v226
	v_permlane16_swap_b32_e32 v223, v227
	v_add_f32_e32 v220, v220, v224
	v_add_f32_e32 v221, v221, v225
	v_add_f32_e32 v222, v222, v226
	v_add_f32_e32 v223, v223, v227
	v_add_f32_dpp v220, v220, v220 row_ror:8 row_mask:0xf bank_mask:0xf
	v_add_f32_dpp v221, v221, v221 row_ror:8 row_mask:0xf bank_mask:0xf
	v_add_f32_dpp v222, v222, v222 row_ror:8 row_mask:0xf bank_mask:0xf
	v_add_f32_dpp v223, v223, v223 row_ror:8 row_mask:0xf bank_mask:0xf
	v_add_f32_dpp v220, v220, v220 row_ror:4 row_mask:0xf bank_mask:0xf
	v_add_f32_dpp v221, v221, v221 row_ror:4 row_mask:0xf bank_mask:0xf
	v_add_f32_dpp v222, v222, v222 row_ror:4 row_mask:0xf bank_mask:0xf
	v_add_f32_dpp v223, v223, v223 row_ror:4 row_mask:0xf bank_mask:0xf
	v_add_f32_dpp v220, v220, v220 row_ror:2 row_mask:0xf bank_mask:0xf
	v_add_f32_dpp v221, v221, v221 row_ror:2 row_mask:0xf bank_mask:0xf
	v_add_f32_dpp v222, v222, v222 row_ror:2 row_mask:0xf bank_mask:0xf
	v_add_f32_dpp v223, v223, v223 row_ror:2 row_mask:0xf bank_mask:0xf
	v_add_f32_dpp v220, v220, v220 row_ror:1 row_mask:0xf bank_mask:0xf
	v_add_f32_dpp v221, v221, v221 row_ror:1 row_mask:0xf bank_mask:0xf
	v_add_f32_dpp v222, v222, v222 row_ror:1 row_mask:0xf bank_mask:0xf
	v_add_f32_dpp v223, v223, v223 row_ror:1 row_mask:0xf bank_mask:0xf
	v_fmamk_f32 v226, v220, 0x3b800000, v7
	v_rsq_f32_e32 v226, v226
	v_lshlrev_b32_e32 v224, 16, v36
	v_lshlrev_b32_e32 v225, 16, v37
	v_mul_f32_e32 v204, v204, v226
	v_mul_f32_e32 v205, v205, v226
	v_mul_f32_e32 v206, v206, v226
	v_mul_f32_e32 v207, v207, v226
	v_mul_f32_e32 v204, v2, v204
	v_mul_f32_e32 v205, v3, v205
	v_mul_f32_e32 v206, v4, v206
	v_mul_f32_e32 v207, v5, v207
	v_and_b32_e32 v36, 0xffff0000, v36
	v_and_b32_e32 v37, 0xffff0000, v37
	v_mul_f32_e32 v226, 0xbfb8aa3b, v224
	v_mul_f32_e32 v227, 0xbfb8aa3b, v36
	v_mul_f32_e32 v1, 0xbfb8aa3b, v225
	v_mul_f32_e32 v220, 0xbfb8aa3b, v37
	v_exp_f32_e32 v226, v226
	v_exp_f32_e32 v227, v227
	v_exp_f32_e32 v1, v1
	v_exp_f32_e32 v220, v220
	v_add_f32_e32 v226, 1.0, v226
	v_add_f32_e32 v227, 1.0, v227
	v_add_f32_e32 v1, 1.0, v1
	v_add_f32_e32 v220, 1.0, v220
	v_rcp_f32_e32 v226, v226
	v_rcp_f32_e32 v227, v227
	v_rcp_f32_e32 v1, v1
	v_rcp_f32_e32 v220, v220
	v_mul_f32_e32 v224, v226, v224
	v_mul_f32_e32 v36, v227, v36
	v_mul_f32_e32 v225, v1, v225
	v_mul_f32_e32 v37, v220, v37
	v_mul_f32_e32 v204, v224, v204
	v_mul_f32_e32 v205, v36, v205
	v_mul_f32_e32 v206, v225, v206
	v_mul_f32_e32 v207, v37, v207
	v_cvt_pk_bf16_f32 v224, v204, v205
	v_cvt_pk_bf16_f32 v225, v206, v207
	s_cmp_gt_i32 s14, 0xffff
	s_cbranch_scc1 .Lgc_skip_a_4
	s_lshr_b32 s17, s14, 2
	s_and_b32 s18, s14, 3
	s_lshl_b32 s17, s17, 12
	s_lshl_b32 s18, s18, 9
	s_add_i32 s17, s17, s18
	v_add_u32_e32 v227, s17, v6
	global_store_dwordx2 v227, v[224:225], s[24:25]
.Lgc_skip_a_4:
	s_add_i32 s14, s14, s9
	v_fmamk_f32 v224, v221, 0x3b800000, v7
	v_rsq_f32_e32 v224, v224
	v_lshlrev_b32_e32 v226, 16, v42
	v_lshlrev_b32_e32 v227, 16, v43
	v_mul_f32_e32 v208, v208, v224
	v_mul_f32_e32 v209, v209, v224
	v_mul_f32_e32 v210, v210, v224
	v_mul_f32_e32 v211, v211, v224
	v_mul_f32_e32 v208, v2, v208
	v_mul_f32_e32 v209, v3, v209
	v_mul_f32_e32 v210, v4, v210
	v_mul_f32_e32 v211, v5, v211
	v_and_b32_e32 v42, 0xffff0000, v42
	v_and_b32_e32 v43, 0xffff0000, v43
	v_mul_f32_e32 v224, 0xbfb8aa3b, v226
	v_mul_f32_e32 v225, 0xbfb8aa3b, v42
	v_mul_f32_e32 v1, 0xbfb8aa3b, v227
	v_mul_f32_e32 v221, 0xbfb8aa3b, v43
	v_exp_f32_e32 v224, v224
	v_exp_f32_e32 v225, v225
	v_exp_f32_e32 v1, v1
	v_exp_f32_e32 v221, v221
	v_add_f32_e32 v224, 1.0, v224
	v_add_f32_e32 v225, 1.0, v225
	v_add_f32_e32 v1, 1.0, v1
	v_add_f32_e32 v221, 1.0, v221
	v_rcp_f32_e32 v224, v224
	v_rcp_f32_e32 v225, v225
	v_rcp_f32_e32 v1, v1
	v_rcp_f32_e32 v221, v221
	v_mul_f32_e32 v226, v224, v226
	v_mul_f32_e32 v42, v225, v42
	v_mul_f32_e32 v227, v1, v227
	v_mul_f32_e32 v43, v221, v43
	v_mul_f32_e32 v208, v226, v208
	v_mul_f32_e32 v209, v42, v209
	v_mul_f32_e32 v210, v227, v210
	v_mul_f32_e32 v211, v43, v211
	v_cvt_pk_bf16_f32 v226, v208, v209
	v_cvt_pk_bf16_f32 v227, v210, v211
	s_cmp_gt_i32 s14, 0xffff
	s_cbranch_scc1 .Lgc_skip_a_5
	s_lshr_b32 s17, s14, 2
	s_and_b32 s18, s14, 3
	s_lshl_b32 s17, s17, 12
	s_lshl_b32 s18, s18, 9
	s_add_i32 s17, s17, s18
	v_add_u32_e32 v225, s17, v6
	global_store_dwordx2 v225, v[226:227], s[24:25]
.Lgc_skip_a_5:
	s_add_i32 s14, s14, s9
	v_fmamk_f32 v226, v222, 0x3b800000, v7
	v_rsq_f32_e32 v226, v226
	v_lshlrev_b32_e32 v224, 16, v48
	v_lshlrev_b32_e32 v225, 16, v49
	v_mul_f32_e32 v212, v212, v226
	v_mul_f32_e32 v213, v213, v226
	v_mul_f32_e32 v214, v214, v226
	v_mul_f32_e32 v215, v215, v226
	v_mul_f32_e32 v212, v2, v212
	v_mul_f32_e32 v213, v3, v213
	v_mul_f32_e32 v214, v4, v214
	v_mul_f32_e32 v215, v5, v215
	v_and_b32_e32 v48, 0xffff0000, v48
	v_and_b32_e32 v49, 0xffff0000, v49
	v_mul_f32_e32 v226, 0xbfb8aa3b, v224
	v_mul_f32_e32 v227, 0xbfb8aa3b, v48
	v_mul_f32_e32 v1, 0xbfb8aa3b, v225
	v_mul_f32_e32 v222, 0xbfb8aa3b, v49
	v_exp_f32_e32 v226, v226
	v_exp_f32_e32 v227, v227
	v_exp_f32_e32 v1, v1
	v_exp_f32_e32 v222, v222
	v_add_f32_e32 v226, 1.0, v226
	v_add_f32_e32 v227, 1.0, v227
	v_add_f32_e32 v1, 1.0, v1
	v_add_f32_e32 v222, 1.0, v222
	v_rcp_f32_e32 v226, v226
	v_rcp_f32_e32 v227, v227
	v_rcp_f32_e32 v1, v1
	v_rcp_f32_e32 v222, v222
	v_mul_f32_e32 v224, v226, v224
	v_mul_f32_e32 v48, v227, v48
	v_mul_f32_e32 v225, v1, v225
	v_mul_f32_e32 v49, v222, v49
	v_mul_f32_e32 v212, v224, v212
	v_mul_f32_e32 v213, v48, v213
	v_mul_f32_e32 v214, v225, v214
	v_mul_f32_e32 v215, v49, v215
	v_cvt_pk_bf16_f32 v224, v212, v213
	v_cvt_pk_bf16_f32 v225, v214, v215
	s_cmp_gt_i32 s14, 0xffff
	s_cbranch_scc1 .Lgc_skip_a_6
	s_lshr_b32 s17, s14, 2
	s_and_b32 s18, s14, 3
	s_lshl_b32 s17, s17, 12
	s_lshl_b32 s18, s18, 9
	s_add_i32 s17, s17, s18
	v_add_u32_e32 v227, s17, v6
	global_store_dwordx2 v227, v[224:225], s[24:25]
.Lgc_skip_a_6:
	s_add_i32 s14, s14, s9
	v_fmamk_f32 v224, v223, 0x3b800000, v7
	v_rsq_f32_e32 v224, v224
	v_lshlrev_b32_e32 v226, 16, v54
	v_lshlrev_b32_e32 v227, 16, v55
	v_mul_f32_e32 v216, v216, v224
	v_mul_f32_e32 v217, v217, v224
	v_mul_f32_e32 v218, v218, v224
	v_mul_f32_e32 v219, v219, v224
	v_mul_f32_e32 v216, v2, v216
	v_mul_f32_e32 v217, v3, v217
	v_mul_f32_e32 v218, v4, v218
	v_mul_f32_e32 v219, v5, v219
	v_and_b32_e32 v54, 0xffff0000, v54
	v_and_b32_e32 v55, 0xffff0000, v55
	v_mul_f32_e32 v224, 0xbfb8aa3b, v226
	v_mul_f32_e32 v225, 0xbfb8aa3b, v54
	v_mul_f32_e32 v1, 0xbfb8aa3b, v227
	v_mul_f32_e32 v223, 0xbfb8aa3b, v55
	v_exp_f32_e32 v224, v224
	v_exp_f32_e32 v225, v225
	v_exp_f32_e32 v1, v1
	v_exp_f32_e32 v223, v223
	v_add_f32_e32 v224, 1.0, v224
	v_add_f32_e32 v225, 1.0, v225
	v_add_f32_e32 v1, 1.0, v1
	v_add_f32_e32 v223, 1.0, v223
	v_rcp_f32_e32 v224, v224
	v_rcp_f32_e32 v225, v225
	v_rcp_f32_e32 v1, v1
	v_rcp_f32_e32 v223, v223
	v_mul_f32_e32 v226, v224, v226
	v_mul_f32_e32 v54, v225, v54
	v_mul_f32_e32 v227, v1, v227
	v_mul_f32_e32 v55, v223, v55
	v_mul_f32_e32 v216, v226, v216
	v_mul_f32_e32 v217, v54, v217
	v_mul_f32_e32 v218, v227, v218
	v_mul_f32_e32 v219, v55, v219
	v_cvt_pk_bf16_f32 v226, v216, v217
	v_cvt_pk_bf16_f32 v227, v218, v219
	s_cmp_gt_i32 s14, 0xffff
	s_cbranch_scc1 .Lgc_skip_a_7
	s_lshr_b32 s17, s14, 2
	s_and_b32 s18, s14, 3
	s_lshl_b32 s17, s17, 12
	s_lshl_b32 s18, s18, 9
	s_add_i32 s17, s17, s18
	v_add_u32_e32 v225, s17, v6
	global_store_dwordx2 v225, v[226:227], s[24:25]
.Lgc_skip_a_7:
	s_add_i32 s14, s14, s9
	v_lshlrev_b32_e32 v204, 16, v56
	v_lshlrev_b32_e32 v224, 16, v58
	v_and_b32_e32 v205, 0xffff0000, v56
	v_and_b32_e32 v225, 0xffff0000, v58
	v_add_f32_e32 v204, v204, v224
	v_add_f32_e32 v205, v205, v225
	v_lshlrev_b32_e32 v206, 16, v57
	v_lshlrev_b32_e32 v224, 16, v59
	v_and_b32_e32 v207, 0xffff0000, v57
	v_and_b32_e32 v225, 0xffff0000, v59
	v_add_f32_e32 v206, v206, v224
	v_add_f32_e32 v207, v207, v225
	v_mul_f32_e32 v224, v204, v204
	v_mul_f32_e32 v225, v205, v205
	v_add_f32_e32 v220, v224, v225
	v_mul_f32_e32 v224, v206, v206
	v_mul_f32_e32 v225, v207, v207
	v_add_f32_e32 v220, v224, v220
	v_add_f32_e32 v220, v225, v220
	v_lshlrev_b32_e32 v208, 16, v62
	v_lshlrev_b32_e32 v226, 16, v64
	v_and_b32_e32 v209, 0xffff0000, v62
	v_and_b32_e32 v227, 0xffff0000, v64
	v_add_f32_e32 v208, v208, v226
	v_add_f32_e32 v209, v209, v227
	v_lshlrev_b32_e32 v210, 16, v63
	v_lshlrev_b32_e32 v226, 16, v65
	v_and_b32_e32 v211, 0xffff0000, v63
	v_and_b32_e32 v227, 0xffff0000, v65
	v_add_f32_e32 v210, v210, v226
	v_add_f32_e32 v211, v211, v227
	v_mul_f32_e32 v226, v208, v208
	v_mul_f32_e32 v227, v209, v209
	v_add_f32_e32 v221, v226, v227
	v_mul_f32_e32 v226, v210, v210
	v_mul_f32_e32 v227, v211, v211
	v_add_f32_e32 v221, v226, v221
	v_add_f32_e32 v221, v227, v221
	v_lshlrev_b32_e32 v212, 16, v68
	v_lshlrev_b32_e32 v224, 16, v70
	v_and_b32_e32 v213, 0xffff0000, v68
	v_and_b32_e32 v225, 0xffff0000, v70
	v_add_f32_e32 v212, v212, v224
	v_add_f32_e32 v213, v213, v225
	v_lshlrev_b32_e32 v214, 16, v69
	v_lshlrev_b32_e32 v224, 16, v71
	v_and_b32_e32 v215, 0xffff0000, v69
	v_and_b32_e32 v225, 0xffff0000, v71
	v_add_f32_e32 v214, v214, v224
	v_add_f32_e32 v215, v215, v225
	v_mul_f32_e32 v224, v212, v212
	v_mul_f32_e32 v225, v213, v213
	v_add_f32_e32 v222, v224, v225
	v_mul_f32_e32 v224, v214, v214
	v_mul_f32_e32 v225, v215, v215
	v_add_f32_e32 v222, v224, v222
	v_add_f32_e32 v222, v225, v222
	v_lshlrev_b32_e32 v216, 16, v74
	v_lshlrev_b32_e32 v226, 16, v76
	v_and_b32_e32 v217, 0xffff0000, v74
	v_and_b32_e32 v227, 0xffff0000, v76
	v_add_f32_e32 v216, v216, v226
	v_add_f32_e32 v217, v217, v227
	v_lshlrev_b32_e32 v218, 16, v75
	v_lshlrev_b32_e32 v226, 16, v77
	v_and_b32_e32 v219, 0xffff0000, v75
	v_and_b32_e32 v227, 0xffff0000, v77
	v_add_f32_e32 v218, v218, v226
	v_add_f32_e32 v219, v219, v227
	v_mul_f32_e32 v226, v216, v216
	v_mul_f32_e32 v227, v217, v217
	v_add_f32_e32 v223, v226, v227
	v_mul_f32_e32 v226, v218, v218
	v_mul_f32_e32 v227, v219, v219
	v_add_f32_e32 v223, v226, v223
	v_add_f32_e32 v223, v227, v223
	v_mov_b32_e32 v224, v220
	v_mov_b32_e32 v225, v221
	v_mov_b32_e32 v226, v222
	v_mov_b32_e32 v227, v223
	v_permlane32_swap_b32_e32 v220, v224
	v_permlane32_swap_b32_e32 v221, v225
	v_permlane32_swap_b32_e32 v222, v226
	v_permlane32_swap_b32_e32 v223, v227
	v_add_f32_e32 v220, v220, v224
	v_add_f32_e32 v221, v221, v225
	v_add_f32_e32 v222, v222, v226
	v_add_f32_e32 v223, v223, v227
	v_mov_b32_e32 v224, v220
	v_mov_b32_e32 v225, v221
	v_mov_b32_e32 v226, v222
	v_mov_b32_e32 v227, v223
	v_permlane16_swap_b32_e32 v220, v224
	v_permlane16_swap_b32_e32 v221, v225
	v_permlane16_swap_b32_e32 v222, v226
	v_permlane16_swap_b32_e32 v223, v227
	v_add_f32_e32 v220, v220, v224
	v_add_f32_e32 v221, v221, v225
	v_add_f32_e32 v222, v222, v226
	v_add_f32_e32 v223, v223, v227
	v_add_f32_dpp v220, v220, v220 row_ror:8 row_mask:0xf bank_mask:0xf
	v_add_f32_dpp v221, v221, v221 row_ror:8 row_mask:0xf bank_mask:0xf
	v_add_f32_dpp v222, v222, v222 row_ror:8 row_mask:0xf bank_mask:0xf
	v_add_f32_dpp v223, v223, v223 row_ror:8 row_mask:0xf bank_mask:0xf
	v_add_f32_dpp v220, v220, v220 row_ror:4 row_mask:0xf bank_mask:0xf
	v_add_f32_dpp v221, v221, v221 row_ror:4 row_mask:0xf bank_mask:0xf
	v_add_f32_dpp v222, v222, v222 row_ror:4 row_mask:0xf bank_mask:0xf
	v_add_f32_dpp v223, v223, v223 row_ror:4 row_mask:0xf bank_mask:0xf
	v_add_f32_dpp v220, v220, v220 row_ror:2 row_mask:0xf bank_mask:0xf
	v_add_f32_dpp v221, v221, v221 row_ror:2 row_mask:0xf bank_mask:0xf
	v_add_f32_dpp v222, v222, v222 row_ror:2 row_mask:0xf bank_mask:0xf
	v_add_f32_dpp v223, v223, v223 row_ror:2 row_mask:0xf bank_mask:0xf
	v_add_f32_dpp v220, v220, v220 row_ror:1 row_mask:0xf bank_mask:0xf
	v_add_f32_dpp v221, v221, v221 row_ror:1 row_mask:0xf bank_mask:0xf
	v_add_f32_dpp v222, v222, v222 row_ror:1 row_mask:0xf bank_mask:0xf
	v_add_f32_dpp v223, v223, v223 row_ror:1 row_mask:0xf bank_mask:0xf
	v_fmamk_f32 v226, v220, 0x3b800000, v7
	v_rsq_f32_e32 v226, v226
	v_lshlrev_b32_e32 v224, 16, v60
	v_lshlrev_b32_e32 v225, 16, v61
	v_mul_f32_e32 v204, v204, v226
	v_mul_f32_e32 v205, v205, v226
	v_mul_f32_e32 v206, v206, v226
	v_mul_f32_e32 v207, v207, v226
	v_mul_f32_e32 v204, v2, v204
	v_mul_f32_e32 v205, v3, v205
	v_mul_f32_e32 v206, v4, v206
	v_mul_f32_e32 v207, v5, v207
	v_and_b32_e32 v60, 0xffff0000, v60
	v_and_b32_e32 v61, 0xffff0000, v61
	v_mul_f32_e32 v226, 0xbfb8aa3b, v224
	v_mul_f32_e32 v227, 0xbfb8aa3b, v60
	v_mul_f32_e32 v1, 0xbfb8aa3b, v225
	v_mul_f32_e32 v220, 0xbfb8aa3b, v61
	v_exp_f32_e32 v226, v226
	v_exp_f32_e32 v227, v227
	v_exp_f32_e32 v1, v1
	v_exp_f32_e32 v220, v220
	v_add_f32_e32 v226, 1.0, v226
	v_add_f32_e32 v227, 1.0, v227
	v_add_f32_e32 v1, 1.0, v1
	v_add_f32_e32 v220, 1.0, v220
	v_rcp_f32_e32 v226, v226
	v_rcp_f32_e32 v227, v227
	v_rcp_f32_e32 v1, v1
	v_rcp_f32_e32 v220, v220
	v_mul_f32_e32 v224, v226, v224
	v_mul_f32_e32 v60, v227, v60
	v_mul_f32_e32 v225, v1, v225
	v_mul_f32_e32 v61, v220, v61
	v_mul_f32_e32 v204, v224, v204
	v_mul_f32_e32 v205, v60, v205
	v_mul_f32_e32 v206, v225, v206
	v_mul_f32_e32 v207, v61, v207
	v_cvt_pk_bf16_f32 v224, v204, v205
	v_cvt_pk_bf16_f32 v225, v206, v207
	s_cmp_gt_i32 s14, 0xffff
	s_cbranch_scc1 .Lgc_skip_a_8
	s_lshr_b32 s17, s14, 2
	s_and_b32 s18, s14, 3
	s_lshl_b32 s17, s17, 12
	s_lshl_b32 s18, s18, 9
	s_add_i32 s17, s17, s18
	v_add_u32_e32 v227, s17, v6
	global_store_dwordx2 v227, v[224:225], s[24:25]
.Lgc_skip_a_8:
	s_add_i32 s14, s14, s9
	v_fmamk_f32 v224, v221, 0x3b800000, v7
	v_rsq_f32_e32 v224, v224
	v_lshlrev_b32_e32 v226, 16, v66
	v_lshlrev_b32_e32 v227, 16, v67
	v_mul_f32_e32 v208, v208, v224
	v_mul_f32_e32 v209, v209, v224
	v_mul_f32_e32 v210, v210, v224
	v_mul_f32_e32 v211, v211, v224
	v_mul_f32_e32 v208, v2, v208
	v_mul_f32_e32 v209, v3, v209
	v_mul_f32_e32 v210, v4, v210
	v_mul_f32_e32 v211, v5, v211
	v_and_b32_e32 v66, 0xffff0000, v66
	v_and_b32_e32 v67, 0xffff0000, v67
	v_mul_f32_e32 v224, 0xbfb8aa3b, v226
	v_mul_f32_e32 v225, 0xbfb8aa3b, v66
	v_mul_f32_e32 v1, 0xbfb8aa3b, v227
	v_mul_f32_e32 v221, 0xbfb8aa3b, v67
	v_exp_f32_e32 v224, v224
	v_exp_f32_e32 v225, v225
	v_exp_f32_e32 v1, v1
	v_exp_f32_e32 v221, v221
	v_add_f32_e32 v224, 1.0, v224
	v_add_f32_e32 v225, 1.0, v225
	v_add_f32_e32 v1, 1.0, v1
	v_add_f32_e32 v221, 1.0, v221
	v_rcp_f32_e32 v224, v224
	v_rcp_f32_e32 v225, v225
	v_rcp_f32_e32 v1, v1
	v_rcp_f32_e32 v221, v221
	v_mul_f32_e32 v226, v224, v226
	v_mul_f32_e32 v66, v225, v66
	v_mul_f32_e32 v227, v1, v227
	v_mul_f32_e32 v67, v221, v67
	v_mul_f32_e32 v208, v226, v208
	v_mul_f32_e32 v209, v66, v209
	v_mul_f32_e32 v210, v227, v210
	v_mul_f32_e32 v211, v67, v211
	v_cvt_pk_bf16_f32 v226, v208, v209
	v_cvt_pk_bf16_f32 v227, v210, v211
	s_cmp_gt_i32 s14, 0xffff
	s_cbranch_scc1 .Lgc_skip_a_9
	s_lshr_b32 s17, s14, 2
	s_and_b32 s18, s14, 3
	s_lshl_b32 s17, s17, 12
	s_lshl_b32 s18, s18, 9
	s_add_i32 s17, s17, s18
	v_add_u32_e32 v225, s17, v6
	global_store_dwordx2 v225, v[226:227], s[24:25]
.Lgc_skip_a_9:
	s_add_i32 s14, s14, s9
	v_fmamk_f32 v226, v222, 0x3b800000, v7
	v_rsq_f32_e32 v226, v226
	v_lshlrev_b32_e32 v224, 16, v72
	v_lshlrev_b32_e32 v225, 16, v73
	v_mul_f32_e32 v212, v212, v226
	v_mul_f32_e32 v213, v213, v226
	v_mul_f32_e32 v214, v214, v226
	v_mul_f32_e32 v215, v215, v226
	v_mul_f32_e32 v212, v2, v212
	v_mul_f32_e32 v213, v3, v213
	v_mul_f32_e32 v214, v4, v214
	v_mul_f32_e32 v215, v5, v215
	v_and_b32_e32 v72, 0xffff0000, v72
	v_and_b32_e32 v73, 0xffff0000, v73
	v_mul_f32_e32 v226, 0xbfb8aa3b, v224
	v_mul_f32_e32 v227, 0xbfb8aa3b, v72
	v_mul_f32_e32 v1, 0xbfb8aa3b, v225
	v_mul_f32_e32 v222, 0xbfb8aa3b, v73
	v_exp_f32_e32 v226, v226
	v_exp_f32_e32 v227, v227
	v_exp_f32_e32 v1, v1
	v_exp_f32_e32 v222, v222
	v_add_f32_e32 v226, 1.0, v226
	v_add_f32_e32 v227, 1.0, v227
	v_add_f32_e32 v1, 1.0, v1
	v_add_f32_e32 v222, 1.0, v222
	v_rcp_f32_e32 v226, v226
	v_rcp_f32_e32 v227, v227
	v_rcp_f32_e32 v1, v1
	v_rcp_f32_e32 v222, v222
	v_mul_f32_e32 v224, v226, v224
	v_mul_f32_e32 v72, v227, v72
	v_mul_f32_e32 v225, v1, v225
	v_mul_f32_e32 v73, v222, v73
	v_mul_f32_e32 v212, v224, v212
	v_mul_f32_e32 v213, v72, v213
	v_mul_f32_e32 v214, v225, v214
	v_mul_f32_e32 v215, v73, v215
	v_cvt_pk_bf16_f32 v224, v212, v213
	v_cvt_pk_bf16_f32 v225, v214, v215
	s_cmp_gt_i32 s14, 0xffff
	s_cbranch_scc1 .Lgc_skip_a_10
	s_lshr_b32 s17, s14, 2
	s_and_b32 s18, s14, 3
	s_lshl_b32 s17, s17, 12
	s_lshl_b32 s18, s18, 9
	s_add_i32 s17, s17, s18
	v_add_u32_e32 v227, s17, v6
	global_store_dwordx2 v227, v[224:225], s[24:25]
.Lgc_skip_a_10:
	s_add_i32 s14, s14, s9
	v_fmamk_f32 v224, v223, 0x3b800000, v7
	v_rsq_f32_e32 v224, v224
	v_lshlrev_b32_e32 v226, 16, v78
	v_lshlrev_b32_e32 v227, 16, v79
	v_mul_f32_e32 v216, v216, v224
	v_mul_f32_e32 v217, v217, v224
	v_mul_f32_e32 v218, v218, v224
	v_mul_f32_e32 v219, v219, v224
	v_mul_f32_e32 v216, v2, v216
	v_mul_f32_e32 v217, v3, v217
	v_mul_f32_e32 v218, v4, v218
	v_mul_f32_e32 v219, v5, v219
	v_and_b32_e32 v78, 0xffff0000, v78
	v_and_b32_e32 v79, 0xffff0000, v79
	v_mul_f32_e32 v224, 0xbfb8aa3b, v226
	v_mul_f32_e32 v225, 0xbfb8aa3b, v78
	v_mul_f32_e32 v1, 0xbfb8aa3b, v227
	v_mul_f32_e32 v223, 0xbfb8aa3b, v79
	v_exp_f32_e32 v224, v224
	v_exp_f32_e32 v225, v225
	v_exp_f32_e32 v1, v1
	v_exp_f32_e32 v223, v223
	v_add_f32_e32 v224, 1.0, v224
	v_add_f32_e32 v225, 1.0, v225
	v_add_f32_e32 v1, 1.0, v1
	v_add_f32_e32 v223, 1.0, v223
	v_rcp_f32_e32 v224, v224
	v_rcp_f32_e32 v225, v225
	v_rcp_f32_e32 v1, v1
	v_rcp_f32_e32 v223, v223
	v_mul_f32_e32 v226, v224, v226
	v_mul_f32_e32 v78, v225, v78
	v_mul_f32_e32 v227, v1, v227
	v_mul_f32_e32 v79, v223, v79
	v_mul_f32_e32 v216, v226, v216
	v_mul_f32_e32 v217, v78, v217
	v_mul_f32_e32 v218, v227, v218
	v_mul_f32_e32 v219, v79, v219
	v_cvt_pk_bf16_f32 v226, v216, v217
	v_cvt_pk_bf16_f32 v227, v218, v219
	s_cmp_gt_i32 s14, 0xffff
	s_cbranch_scc1 .Lgc_skip_a_11
	s_lshr_b32 s17, s14, 2
	s_and_b32 s18, s14, 3
	s_lshl_b32 s17, s17, 12
	s_lshl_b32 s18, s18, 9
	s_add_i32 s17, s17, s18
	v_add_u32_e32 v225, s17, v6
	global_store_dwordx2 v225, v[226:227], s[24:25]
.Lgc_skip_a_11:
	s_add_i32 s14, s14, s9
	v_lshlrev_b32_e32 v204, 16, v80
	v_lshlrev_b32_e32 v224, 16, v82
	v_and_b32_e32 v205, 0xffff0000, v80
	v_and_b32_e32 v225, 0xffff0000, v82
	v_add_f32_e32 v204, v204, v224
	v_add_f32_e32 v205, v205, v225
	v_lshlrev_b32_e32 v206, 16, v81
	v_lshlrev_b32_e32 v224, 16, v83
	v_and_b32_e32 v207, 0xffff0000, v81
	v_and_b32_e32 v225, 0xffff0000, v83
	v_add_f32_e32 v206, v206, v224
	v_add_f32_e32 v207, v207, v225
	v_mul_f32_e32 v224, v204, v204
	v_mul_f32_e32 v225, v205, v205
	v_add_f32_e32 v220, v224, v225
	v_mul_f32_e32 v224, v206, v206
	v_mul_f32_e32 v225, v207, v207
	v_add_f32_e32 v220, v224, v220
	v_add_f32_e32 v220, v225, v220
	v_lshlrev_b32_e32 v208, 16, v86
	v_lshlrev_b32_e32 v226, 16, v88
	v_and_b32_e32 v209, 0xffff0000, v86
	v_and_b32_e32 v227, 0xffff0000, v88
	v_add_f32_e32 v208, v208, v226
	v_add_f32_e32 v209, v209, v227
	v_lshlrev_b32_e32 v210, 16, v87
	v_lshlrev_b32_e32 v226, 16, v89
	v_and_b32_e32 v211, 0xffff0000, v87
	v_and_b32_e32 v227, 0xffff0000, v89
	v_add_f32_e32 v210, v210, v226
	v_add_f32_e32 v211, v211, v227
	v_mul_f32_e32 v226, v208, v208
	v_mul_f32_e32 v227, v209, v209
	v_add_f32_e32 v221, v226, v227
	v_mul_f32_e32 v226, v210, v210
	v_mul_f32_e32 v227, v211, v211
	v_add_f32_e32 v221, v226, v221
	v_add_f32_e32 v221, v227, v221
	v_lshlrev_b32_e32 v212, 16, v92
	v_lshlrev_b32_e32 v224, 16, v94
	v_and_b32_e32 v213, 0xffff0000, v92
	v_and_b32_e32 v225, 0xffff0000, v94
	v_add_f32_e32 v212, v212, v224
	v_add_f32_e32 v213, v213, v225
	v_lshlrev_b32_e32 v214, 16, v93
	v_lshlrev_b32_e32 v224, 16, v95
	v_and_b32_e32 v215, 0xffff0000, v93
	v_and_b32_e32 v225, 0xffff0000, v95
	v_add_f32_e32 v214, v214, v224
	v_add_f32_e32 v215, v215, v225
	v_mul_f32_e32 v224, v212, v212
	v_mul_f32_e32 v225, v213, v213
	v_add_f32_e32 v222, v224, v225
	v_mul_f32_e32 v224, v214, v214
	v_mul_f32_e32 v225, v215, v215
	v_add_f32_e32 v222, v224, v222
	v_add_f32_e32 v222, v225, v222
	v_lshlrev_b32_e32 v216, 16, v98
	v_lshlrev_b32_e32 v226, 16, v100
	v_and_b32_e32 v217, 0xffff0000, v98
	v_and_b32_e32 v227, 0xffff0000, v100
	v_add_f32_e32 v216, v216, v226
	v_add_f32_e32 v217, v217, v227
	v_lshlrev_b32_e32 v218, 16, v99
	v_lshlrev_b32_e32 v226, 16, v101
	v_and_b32_e32 v219, 0xffff0000, v99
	v_and_b32_e32 v227, 0xffff0000, v101
	v_add_f32_e32 v218, v218, v226
	v_add_f32_e32 v219, v219, v227
	v_mul_f32_e32 v226, v216, v216
	v_mul_f32_e32 v227, v217, v217
	v_add_f32_e32 v223, v226, v227
	v_mul_f32_e32 v226, v218, v218
	v_mul_f32_e32 v227, v219, v219
	v_add_f32_e32 v223, v226, v223
	v_add_f32_e32 v223, v227, v223
	v_mov_b32_e32 v224, v220
	v_mov_b32_e32 v225, v221
	v_mov_b32_e32 v226, v222
	v_mov_b32_e32 v227, v223
	v_permlane32_swap_b32_e32 v220, v224
	v_permlane32_swap_b32_e32 v221, v225
	v_permlane32_swap_b32_e32 v222, v226
	v_permlane32_swap_b32_e32 v223, v227
	v_add_f32_e32 v220, v220, v224
	v_add_f32_e32 v221, v221, v225
	v_add_f32_e32 v222, v222, v226
	v_add_f32_e32 v223, v223, v227
	v_mov_b32_e32 v224, v220
	v_mov_b32_e32 v225, v221
	v_mov_b32_e32 v226, v222
	v_mov_b32_e32 v227, v223
	v_permlane16_swap_b32_e32 v220, v224
	v_permlane16_swap_b32_e32 v221, v225
	v_permlane16_swap_b32_e32 v222, v226
	v_permlane16_swap_b32_e32 v223, v227
	v_add_f32_e32 v220, v220, v224
	v_add_f32_e32 v221, v221, v225
	v_add_f32_e32 v222, v222, v226
	v_add_f32_e32 v223, v223, v227
	v_add_f32_dpp v220, v220, v220 row_ror:8 row_mask:0xf bank_mask:0xf
	v_add_f32_dpp v221, v221, v221 row_ror:8 row_mask:0xf bank_mask:0xf
	v_add_f32_dpp v222, v222, v222 row_ror:8 row_mask:0xf bank_mask:0xf
	v_add_f32_dpp v223, v223, v223 row_ror:8 row_mask:0xf bank_mask:0xf
	v_add_f32_dpp v220, v220, v220 row_ror:4 row_mask:0xf bank_mask:0xf
	v_add_f32_dpp v221, v221, v221 row_ror:4 row_mask:0xf bank_mask:0xf
	v_add_f32_dpp v222, v222, v222 row_ror:4 row_mask:0xf bank_mask:0xf
	v_add_f32_dpp v223, v223, v223 row_ror:4 row_mask:0xf bank_mask:0xf
	v_add_f32_dpp v220, v220, v220 row_ror:2 row_mask:0xf bank_mask:0xf
	v_add_f32_dpp v221, v221, v221 row_ror:2 row_mask:0xf bank_mask:0xf
	v_add_f32_dpp v222, v222, v222 row_ror:2 row_mask:0xf bank_mask:0xf
	v_add_f32_dpp v223, v223, v223 row_ror:2 row_mask:0xf bank_mask:0xf
	v_add_f32_dpp v220, v220, v220 row_ror:1 row_mask:0xf bank_mask:0xf
	v_add_f32_dpp v221, v221, v221 row_ror:1 row_mask:0xf bank_mask:0xf
	v_add_f32_dpp v222, v222, v222 row_ror:1 row_mask:0xf bank_mask:0xf
	v_add_f32_dpp v223, v223, v223 row_ror:1 row_mask:0xf bank_mask:0xf
	v_fmamk_f32 v226, v220, 0x3b800000, v7
	v_rsq_f32_e32 v226, v226
	v_lshlrev_b32_e32 v224, 16, v84
	v_lshlrev_b32_e32 v225, 16, v85
	v_mul_f32_e32 v204, v204, v226
	v_mul_f32_e32 v205, v205, v226
	v_mul_f32_e32 v206, v206, v226
	v_mul_f32_e32 v207, v207, v226
	v_mul_f32_e32 v204, v2, v204
	v_mul_f32_e32 v205, v3, v205
	v_mul_f32_e32 v206, v4, v206
	v_mul_f32_e32 v207, v5, v207
	v_and_b32_e32 v84, 0xffff0000, v84
	v_and_b32_e32 v85, 0xffff0000, v85
	v_mul_f32_e32 v226, 0xbfb8aa3b, v224
	v_mul_f32_e32 v227, 0xbfb8aa3b, v84
	v_mul_f32_e32 v1, 0xbfb8aa3b, v225
	v_mul_f32_e32 v220, 0xbfb8aa3b, v85
	v_exp_f32_e32 v226, v226
	v_exp_f32_e32 v227, v227
	v_exp_f32_e32 v1, v1
	v_exp_f32_e32 v220, v220
	v_add_f32_e32 v226, 1.0, v226
	v_add_f32_e32 v227, 1.0, v227
	v_add_f32_e32 v1, 1.0, v1
	v_add_f32_e32 v220, 1.0, v220
	v_rcp_f32_e32 v226, v226
	v_rcp_f32_e32 v227, v227
	v_rcp_f32_e32 v1, v1
	v_rcp_f32_e32 v220, v220
	v_mul_f32_e32 v224, v226, v224
	v_mul_f32_e32 v84, v227, v84
	v_mul_f32_e32 v225, v1, v225
	v_mul_f32_e32 v85, v220, v85
	v_mul_f32_e32 v204, v224, v204
	v_mul_f32_e32 v205, v84, v205
	v_mul_f32_e32 v206, v225, v206
	v_mul_f32_e32 v207, v85, v207
	v_cvt_pk_bf16_f32 v224, v204, v205
	v_cvt_pk_bf16_f32 v225, v206, v207
	s_cmp_gt_i32 s14, 0xffff
	s_cbranch_scc1 .Lgc_skip_a_12
	s_lshr_b32 s17, s14, 2
	s_and_b32 s18, s14, 3
	s_lshl_b32 s17, s17, 12
	s_lshl_b32 s18, s18, 9
	s_add_i32 s17, s17, s18
	v_add_u32_e32 v227, s17, v6
	global_store_dwordx2 v227, v[224:225], s[24:25]
.Lgc_skip_a_12:
	s_add_i32 s14, s14, s9
	v_fmamk_f32 v224, v221, 0x3b800000, v7
	v_rsq_f32_e32 v224, v224
	v_lshlrev_b32_e32 v226, 16, v90
	v_lshlrev_b32_e32 v227, 16, v91
	v_mul_f32_e32 v208, v208, v224
	v_mul_f32_e32 v209, v209, v224
	v_mul_f32_e32 v210, v210, v224
	v_mul_f32_e32 v211, v211, v224
	v_mul_f32_e32 v208, v2, v208
	v_mul_f32_e32 v209, v3, v209
	v_mul_f32_e32 v210, v4, v210
	v_mul_f32_e32 v211, v5, v211
	v_and_b32_e32 v90, 0xffff0000, v90
	v_and_b32_e32 v91, 0xffff0000, v91
	v_mul_f32_e32 v224, 0xbfb8aa3b, v226
	v_mul_f32_e32 v225, 0xbfb8aa3b, v90
	v_mul_f32_e32 v1, 0xbfb8aa3b, v227
	v_mul_f32_e32 v221, 0xbfb8aa3b, v91
	v_exp_f32_e32 v224, v224
	v_exp_f32_e32 v225, v225
	v_exp_f32_e32 v1, v1
	v_exp_f32_e32 v221, v221
	v_add_f32_e32 v224, 1.0, v224
	v_add_f32_e32 v225, 1.0, v225
	v_add_f32_e32 v1, 1.0, v1
	v_add_f32_e32 v221, 1.0, v221
	v_rcp_f32_e32 v224, v224
	v_rcp_f32_e32 v225, v225
	v_rcp_f32_e32 v1, v1
	v_rcp_f32_e32 v221, v221
	v_mul_f32_e32 v226, v224, v226
	v_mul_f32_e32 v90, v225, v90
	v_mul_f32_e32 v227, v1, v227
	v_mul_f32_e32 v91, v221, v91
	v_mul_f32_e32 v208, v226, v208
	v_mul_f32_e32 v209, v90, v209
	v_mul_f32_e32 v210, v227, v210
	v_mul_f32_e32 v211, v91, v211
	v_cvt_pk_bf16_f32 v226, v208, v209
	v_cvt_pk_bf16_f32 v227, v210, v211
	s_cmp_gt_i32 s14, 0xffff
	s_cbranch_scc1 .Lgc_skip_a_13
	s_lshr_b32 s17, s14, 2
	s_and_b32 s18, s14, 3
	s_lshl_b32 s17, s17, 12
	s_lshl_b32 s18, s18, 9
	s_add_i32 s17, s17, s18
	v_add_u32_e32 v225, s17, v6
	global_store_dwordx2 v225, v[226:227], s[24:25]
.Lgc_skip_a_13:
	s_add_i32 s14, s14, s9
	v_fmamk_f32 v226, v222, 0x3b800000, v7
	v_rsq_f32_e32 v226, v226
	v_lshlrev_b32_e32 v224, 16, v96
	v_lshlrev_b32_e32 v225, 16, v97
	v_mul_f32_e32 v212, v212, v226
	v_mul_f32_e32 v213, v213, v226
	v_mul_f32_e32 v214, v214, v226
	v_mul_f32_e32 v215, v215, v226
	v_mul_f32_e32 v212, v2, v212
	v_mul_f32_e32 v213, v3, v213
	v_mul_f32_e32 v214, v4, v214
	v_mul_f32_e32 v215, v5, v215
	v_and_b32_e32 v96, 0xffff0000, v96
	v_and_b32_e32 v97, 0xffff0000, v97
	v_mul_f32_e32 v226, 0xbfb8aa3b, v224
	v_mul_f32_e32 v227, 0xbfb8aa3b, v96
	v_mul_f32_e32 v1, 0xbfb8aa3b, v225
	v_mul_f32_e32 v222, 0xbfb8aa3b, v97
	v_exp_f32_e32 v226, v226
	v_exp_f32_e32 v227, v227
	v_exp_f32_e32 v1, v1
	v_exp_f32_e32 v222, v222
	v_add_f32_e32 v226, 1.0, v226
	v_add_f32_e32 v227, 1.0, v227
	v_add_f32_e32 v1, 1.0, v1
	v_add_f32_e32 v222, 1.0, v222
	v_rcp_f32_e32 v226, v226
	v_rcp_f32_e32 v227, v227
	v_rcp_f32_e32 v1, v1
	v_rcp_f32_e32 v222, v222
	v_mul_f32_e32 v224, v226, v224
	v_mul_f32_e32 v96, v227, v96
	v_mul_f32_e32 v225, v1, v225
	v_mul_f32_e32 v97, v222, v97
	v_mul_f32_e32 v212, v224, v212
	v_mul_f32_e32 v213, v96, v213
	v_mul_f32_e32 v214, v225, v214
	v_mul_f32_e32 v215, v97, v215
	v_cvt_pk_bf16_f32 v224, v212, v213
	v_cvt_pk_bf16_f32 v225, v214, v215
	s_cmp_gt_i32 s14, 0xffff
	s_cbranch_scc1 .Lgc_skip_a_14
	s_lshr_b32 s17, s14, 2
	s_and_b32 s18, s14, 3
	s_lshl_b32 s17, s17, 12
	s_lshl_b32 s18, s18, 9
	s_add_i32 s17, s17, s18
	v_add_u32_e32 v227, s17, v6
	global_store_dwordx2 v227, v[224:225], s[24:25]
.Lgc_skip_a_14:
	s_add_i32 s14, s14, s9
	v_fmamk_f32 v224, v223, 0x3b800000, v7
	v_rsq_f32_e32 v224, v224
	v_lshlrev_b32_e32 v226, 16, v102
	v_lshlrev_b32_e32 v227, 16, v103
	v_mul_f32_e32 v216, v216, v224
	v_mul_f32_e32 v217, v217, v224
	v_mul_f32_e32 v218, v218, v224
	v_mul_f32_e32 v219, v219, v224
	v_mul_f32_e32 v216, v2, v216
	v_mul_f32_e32 v217, v3, v217
	v_mul_f32_e32 v218, v4, v218
	v_mul_f32_e32 v219, v5, v219
	v_and_b32_e32 v102, 0xffff0000, v102
	v_and_b32_e32 v103, 0xffff0000, v103
	v_mul_f32_e32 v224, 0xbfb8aa3b, v226
	v_mul_f32_e32 v225, 0xbfb8aa3b, v102
	v_mul_f32_e32 v1, 0xbfb8aa3b, v227
	v_mul_f32_e32 v223, 0xbfb8aa3b, v103
	v_exp_f32_e32 v224, v224
	v_exp_f32_e32 v225, v225
	v_exp_f32_e32 v1, v1
	v_exp_f32_e32 v223, v223
	v_add_f32_e32 v224, 1.0, v224
	v_add_f32_e32 v225, 1.0, v225
	v_add_f32_e32 v1, 1.0, v1
	v_add_f32_e32 v223, 1.0, v223
	v_rcp_f32_e32 v224, v224
	v_rcp_f32_e32 v225, v225
	v_rcp_f32_e32 v1, v1
	v_rcp_f32_e32 v223, v223
	v_mul_f32_e32 v226, v224, v226
	v_mul_f32_e32 v102, v225, v102
	v_mul_f32_e32 v227, v1, v227
	v_mul_f32_e32 v103, v223, v103
	v_mul_f32_e32 v216, v226, v216
	v_mul_f32_e32 v217, v102, v217
	v_mul_f32_e32 v218, v227, v218
	v_mul_f32_e32 v219, v103, v219
	v_cvt_pk_bf16_f32 v226, v216, v217
	v_cvt_pk_bf16_f32 v227, v218, v219
	s_cmp_gt_i32 s14, 0xffff
	s_cbranch_scc1 .Lgc_skip_a_15
	s_lshr_b32 s17, s14, 2
	s_and_b32 s18, s14, 3
	s_lshl_b32 s17, s17, 12
	s_lshl_b32 s18, s18, 9
	s_add_i32 s17, s17, s18
	v_add_u32_e32 v225, s17, v6
	global_store_dwordx2 v225, v[226:227], s[24:25]
.Lgc_skip_a_15:
	s_mov_b32 s10, s19
	s_cmp_gt_i32 s10, 0xffff
	s_cbranch_scc1 .Lgc_done
	s_add_i32 s19, s10, s11
	s_mov_b32 s14, s19
	s_min_i32 s15, s14, 0xffff
	s_lshl_b32 s16, s15, 9
	s_lshr_b32 s17, s15, 2
	s_and_b32 s18, s15, 3
	s_mul_i32 s17, s17, 0x3200
	s_lshl_b32 s18, s18, 9
	s_add_i32 s17, s17, s18
	v_add_u32_e32 v224, s16, v6
	v_add_u32_e32 v225, s17, v6
	global_load_dwordx2 v[8:9], v224, s[0:1]
	global_load_dwordx2 v[10:11], v224, s[4:5]
	global_load_dwordx2 v[12:13], v225, s[22:23]
	s_add_i32 s14, s14, s9
	s_min_i32 s15, s14, 0xffff
	s_lshl_b32 s16, s15, 9
	s_lshr_b32 s17, s15, 2
	s_and_b32 s18, s15, 3
	s_mul_i32 s17, s17, 0x3200
	s_lshl_b32 s18, s18, 9
	s_add_i32 s17, s17, s18
	v_add_u32_e32 v226, s16, v6
	v_add_u32_e32 v227, s17, v6
	global_load_dwordx2 v[14:15], v226, s[0:1]
	global_load_dwordx2 v[16:17], v226, s[4:5]
	global_load_dwordx2 v[18:19], v227, s[22:23]
	s_add_i32 s14, s14, s9
	s_min_i32 s15, s14, 0xffff
	s_lshl_b32 s16, s15, 9
	s_lshr_b32 s17, s15, 2
	s_and_b32 s18, s15, 3
	s_mul_i32 s17, s17, 0x3200
	s_lshl_b32 s18, s18, 9
	s_add_i32 s17, s17, s18
	v_add_u32_e32 v224, s16, v6
	v_add_u32_e32 v225, s17, v6
	global_load_dwordx2 v[20:21], v224, s[0:1]
	global_load_dwordx2 v[22:23], v224, s[4:5]
	global_load_dwordx2 v[24:25], v225, s[22:23]
	s_add_i32 s14, s14, s9
	s_min_i32 s15, s14, 0xffff
	s_lshl_b32 s16, s15, 9
	s_lshr_b32 s17, s15, 2
	s_and_b32 s18, s15, 3
	s_mul_i32 s17, s17, 0x3200
	s_lshl_b32 s18, s18, 9
	s_add_i32 s17, s17, s18
	v_add_u32_e32 v226, s16, v6
	v_add_u32_e32 v227, s17, v6
	global_load_dwordx2 v[26:27], v226, s[0:1]
	global_load_dwordx2 v[28:29], v226, s[4:5]
	global_load_dwordx2 v[30:31], v227, s[22:23]
	s_add_i32 s14, s14, s9
	s_min_i32 s15, s14, 0xffff
	s_lshl_b32 s16, s15, 9
	s_lshr_b32 s17, s15, 2
	s_and_b32 s18, s15, 3
	s_mul_i32 s17, s17, 0x3200
	s_lshl_b32 s18, s18, 9
	s_add_i32 s17, s17, s18
	v_add_u32_e32 v224, s16, v6
	v_add_u32_e32 v225, s17, v6
	global_load_dwordx2 v[32:33], v224, s[0:1]
	global_load_dwordx2 v[34:35], v224, s[4:5]
	global_load_dwordx2 v[36:37], v225, s[22:23]
	s_add_i32 s14, s14, s9
	s_min_i32 s15, s14, 0xffff
	s_lshl_b32 s16, s15, 9
	s_lshr_b32 s17, s15, 2
	s_and_b32 s18, s15, 3
	s_mul_i32 s17, s17, 0x3200
	s_lshl_b32 s18, s18, 9
	s_add_i32 s17, s17, s18
	v_add_u32_e32 v226, s16, v6
	v_add_u32_e32 v227, s17, v6
	global_load_dwordx2 v[38:39], v226, s[0:1]
	global_load_dwordx2 v[40:41], v226, s[4:5]
	global_load_dwordx2 v[42:43], v227, s[22:23]
	s_add_i32 s14, s14, s9
	s_min_i32 s15, s14, 0xffff
	s_lshl_b32 s16, s15, 9
	s_lshr_b32 s17, s15, 2
	s_and_b32 s18, s15, 3
	s_mul_i32 s17, s17, 0x3200
	s_lshl_b32 s18, s18, 9
	s_add_i32 s17, s17, s18
	v_add_u32_e32 v224, s16, v6
	v_add_u32_e32 v225, s17, v6
	global_load_dwordx2 v[44:45], v224, s[0:1]
	global_load_dwordx2 v[46:47], v224, s[4:5]
	global_load_dwordx2 v[48:49], v225, s[22:23]
	s_add_i32 s14, s14, s9
	s_min_i32 s15, s14, 0xffff
	s_lshl_b32 s16, s15, 9
	s_lshr_b32 s17, s15, 2
	s_and_b32 s18, s15, 3
	s_mul_i32 s17, s17, 0x3200
	s_lshl_b32 s18, s18, 9
	s_add_i32 s17, s17, s18
	v_add_u32_e32 v226, s16, v6
	v_add_u32_e32 v227, s17, v6
	global_load_dwordx2 v[50:51], v226, s[0:1]
	global_load_dwordx2 v[52:53], v226, s[4:5]
	global_load_dwordx2 v[54:55], v227, s[22:23]
	s_add_i32 s14, s14, s9
	s_min_i32 s15, s14, 0xffff
	s_lshl_b32 s16, s15, 9
	s_lshr_b32 s17, s15, 2
	s_and_b32 s18, s15, 3
	s_mul_i32 s17, s17, 0x3200
	s_lshl_b32 s18, s18, 9
	s_add_i32 s17, s17, s18
	v_add_u32_e32 v224, s16, v6
	v_add_u32_e32 v225, s17, v6
	global_load_dwordx2 v[56:57], v224, s[0:1]
	global_load_dwordx2 v[58:59], v224, s[4:5]
	global_load_dwordx2 v[60:61], v225, s[22:23]
	s_add_i32 s14, s14, s9
	s_min_i32 s15, s14, 0xffff
	s_lshl_b32 s16, s15, 9
	s_lshr_b32 s17, s15, 2
	s_and_b32 s18, s15, 3
	s_mul_i32 s17, s17, 0x3200
	s_lshl_b32 s18, s18, 9
	s_add_i32 s17, s17, s18
	v_add_u32_e32 v226, s16, v6
	v_add_u32_e32 v227, s17, v6
	global_load_dwordx2 v[62:63], v226, s[0:1]
	global_load_dwordx2 v[64:65], v226, s[4:5]
	global_load_dwordx2 v[66:67], v227, s[22:23]
	s_add_i32 s14, s14, s9
	s_min_i32 s15, s14, 0xffff
	s_lshl_b32 s16, s15, 9
	s_lshr_b32 s17, s15, 2
	s_and_b32 s18, s15, 3
	s_mul_i32 s17, s17, 0x3200
	s_lshl_b32 s18, s18, 9
	s_add_i32 s17, s17, s18
	v_add_u32_e32 v224, s16, v6
	v_add_u32_e32 v225, s17, v6
	global_load_dwordx2 v[68:69], v224, s[0:1]
	global_load_dwordx2 v[70:71], v224, s[4:5]
	global_load_dwordx2 v[72:73], v225, s[22:23]
	s_add_i32 s14, s14, s9
	s_min_i32 s15, s14, 0xffff
	s_lshl_b32 s16, s15, 9
	s_lshr_b32 s17, s15, 2
	s_and_b32 s18, s15, 3
	s_mul_i32 s17, s17, 0x3200
	s_lshl_b32 s18, s18, 9
	s_add_i32 s17, s17, s18
	v_add_u32_e32 v226, s16, v6
	v_add_u32_e32 v227, s17, v6
	global_load_dwordx2 v[74:75], v226, s[0:1]
	global_load_dwordx2 v[76:77], v226, s[4:5]
	global_load_dwordx2 v[78:79], v227, s[22:23]
	s_add_i32 s14, s14, s9
	s_min_i32 s15, s14, 0xffff
	s_lshl_b32 s16, s15, 9
	s_lshr_b32 s17, s15, 2
	s_and_b32 s18, s15, 3
	s_mul_i32 s17, s17, 0x3200
	s_lshl_b32 s18, s18, 9
	s_add_i32 s17, s17, s18
	v_add_u32_e32 v224, s16, v6
	v_add_u32_e32 v225, s17, v6
	global_load_dwordx2 v[80:81], v224, s[0:1]
	global_load_dwordx2 v[82:83], v224, s[4:5]
	global_load_dwordx2 v[84:85], v225, s[22:23]
	s_add_i32 s14, s14, s9
	s_min_i32 s15, s14, 0xffff
	s_lshl_b32 s16, s15, 9
	s_lshr_b32 s17, s15, 2
	s_and_b32 s18, s15, 3
	s_mul_i32 s17, s17, 0x3200
	s_lshl_b32 s18, s18, 9
	s_add_i32 s17, s17, s18
	v_add_u32_e32 v226, s16, v6
	v_add_u32_e32 v227, s17, v6
	global_load_dwordx2 v[86:87], v226, s[0:1]
	global_load_dwordx2 v[88:89], v226, s[4:5]
	global_load_dwordx2 v[90:91], v227, s[22:23]
	s_add_i32 s14, s14, s9
	s_min_i32 s15, s14, 0xffff
	s_lshl_b32 s16, s15, 9
	s_lshr_b32 s17, s15, 2
	s_and_b32 s18, s15, 3
	s_mul_i32 s17, s17, 0x3200
	s_lshl_b32 s18, s18, 9
	s_add_i32 s17, s17, s18
	v_add_u32_e32 v224, s16, v6
	v_add_u32_e32 v225, s17, v6
	global_load_dwordx2 v[92:93], v224, s[0:1]
	global_load_dwordx2 v[94:95], v224, s[4:5]
	global_load_dwordx2 v[96:97], v225, s[22:23]
	s_add_i32 s14, s14, s9
	s_min_i32 s15, s14, 0xffff
	s_lshl_b32 s16, s15, 9
	s_lshr_b32 s17, s15, 2
	s_and_b32 s18, s15, 3
	s_mul_i32 s17, s17, 0x3200
	s_lshl_b32 s18, s18, 9
	s_add_i32 s17, s17, s18
	v_add_u32_e32 v226, s16, v6
	v_add_u32_e32 v227, s17, v6
	global_load_dwordx2 v[98:99], v226, s[0:1]
	global_load_dwordx2 v[100:101], v226, s[4:5]
	global_load_dwordx2 v[102:103], v227, s[22:23]
	s_waitcnt vmcnt(48)
	s_mov_b32 s14, s10
	v_lshlrev_b32_e32 v204, 16, v104
	v_lshlrev_b32_e32 v224, 16, v106
	v_and_b32_e32 v205, 0xffff0000, v104
	v_and_b32_e32 v225, 0xffff0000, v106
	v_add_f32_e32 v204, v204, v224
	v_add_f32_e32 v205, v205, v225
	v_lshlrev_b32_e32 v206, 16, v105
	v_lshlrev_b32_e32 v224, 16, v107
	v_and_b32_e32 v207, 0xffff0000, v105
	v_and_b32_e32 v225, 0xffff0000, v107
	v_add_f32_e32 v206, v206, v224
	v_add_f32_e32 v207, v207, v225
	v_mul_f32_e32 v224, v204, v204
	v_mul_f32_e32 v225, v205, v205
	v_add_f32_e32 v220, v224, v225
	v_mul_f32_e32 v224, v206, v206
	v_mul_f32_e32 v225, v207, v207
	v_add_f32_e32 v220, v224, v220
	v_add_f32_e32 v220, v225, v220
	v_lshlrev_b32_e32 v208, 16, v110
	v_lshlrev_b32_e32 v226, 16, v112
	v_and_b32_e32 v209, 0xffff0000, v110
	v_and_b32_e32 v227, 0xffff0000, v112
	v_add_f32_e32 v208, v208, v226
	v_add_f32_e32 v209, v209, v227
	v_lshlrev_b32_e32 v210, 16, v111
	v_lshlrev_b32_e32 v226, 16, v113
	v_and_b32_e32 v211, 0xffff0000, v111
	v_and_b32_e32 v227, 0xffff0000, v113
	v_add_f32_e32 v210, v210, v226
	v_add_f32_e32 v211, v211, v227
	v_mul_f32_e32 v226, v208, v208
	v_mul_f32_e32 v227, v209, v209
	v_add_f32_e32 v221, v226, v227
	v_mul_f32_e32 v226, v210, v210
	v_mul_f32_e32 v227, v211, v211
	v_add_f32_e32 v221, v226, v221
	v_add_f32_e32 v221, v227, v221
	v_lshlrev_b32_e32 v212, 16, v116
	v_lshlrev_b32_e32 v224, 16, v118
	v_and_b32_e32 v213, 0xffff0000, v116
	v_and_b32_e32 v225, 0xffff0000, v118
	v_add_f32_e32 v212, v212, v224
	v_add_f32_e32 v213, v213, v225
	v_lshlrev_b32_e32 v214, 16, v117
	v_lshlrev_b32_e32 v224, 16, v119
	v_and_b32_e32 v215, 0xffff0000, v117
	v_and_b32_e32 v225, 0xffff0000, v119
	v_add_f32_e32 v214, v214, v224
	v_add_f32_e32 v215, v215, v225
	v_mul_f32_e32 v224, v212, v212
	v_mul_f32_e32 v225, v213, v213
	v_add_f32_e32 v222, v224, v225
	v_mul_f32_e32 v224, v214, v214
	v_mul_f32_e32 v225, v215, v215
	v_add_f32_e32 v222, v224, v222
	v_add_f32_e32 v222, v225, v222
	v_lshlrev_b32_e32 v216, 16, v122
	v_lshlrev_b32_e32 v226, 16, v124
	v_and_b32_e32 v217, 0xffff0000, v122
	v_and_b32_e32 v227, 0xffff0000, v124
	v_add_f32_e32 v216, v216, v226
	v_add_f32_e32 v217, v217, v227
	v_lshlrev_b32_e32 v218, 16, v123
	v_lshlrev_b32_e32 v226, 16, v125
	v_and_b32_e32 v219, 0xffff0000, v123
	v_and_b32_e32 v227, 0xffff0000, v125
	v_add_f32_e32 v218, v218, v226
	v_add_f32_e32 v219, v219, v227
	v_mul_f32_e32 v226, v216, v216
	v_mul_f32_e32 v227, v217, v217
	v_add_f32_e32 v223, v226, v227
	v_mul_f32_e32 v226, v218, v218
	v_mul_f32_e32 v227, v219, v219
	v_add_f32_e32 v223, v226, v223
	v_add_f32_e32 v223, v227, v223
	v_mov_b32_e32 v224, v220
	v_mov_b32_e32 v225, v221
	v_mov_b32_e32 v226, v222
	v_mov_b32_e32 v227, v223
	v_permlane32_swap_b32_e32 v220, v224
	v_permlane32_swap_b32_e32 v221, v225
	v_permlane32_swap_b32_e32 v222, v226
	v_permlane32_swap_b32_e32 v223, v227
	v_add_f32_e32 v220, v220, v224
	v_add_f32_e32 v221, v221, v225
	v_add_f32_e32 v222, v222, v226
	v_add_f32_e32 v223, v223, v227
	v_mov_b32_e32 v224, v220
	v_mov_b32_e32 v225, v221
	v_mov_b32_e32 v226, v222
	v_mov_b32_e32 v227, v223
	v_permlane16_swap_b32_e32 v220, v224
	v_permlane16_swap_b32_e32 v221, v225
	v_permlane16_swap_b32_e32 v222, v226
	v_permlane16_swap_b32_e32 v223, v227
	v_add_f32_e32 v220, v220, v224
	v_add_f32_e32 v221, v221, v225
	v_add_f32_e32 v222, v222, v226
	v_add_f32_e32 v223, v223, v227
	v_add_f32_dpp v220, v220, v220 row_ror:8 row_mask:0xf bank_mask:0xf
	v_add_f32_dpp v221, v221, v221 row_ror:8 row_mask:0xf bank_mask:0xf
	v_add_f32_dpp v222, v222, v222 row_ror:8 row_mask:0xf bank_mask:0xf
	v_add_f32_dpp v223, v223, v223 row_ror:8 row_mask:0xf bank_mask:0xf
	v_add_f32_dpp v220, v220, v220 row_ror:4 row_mask:0xf bank_mask:0xf
	v_add_f32_dpp v221, v221, v221 row_ror:4 row_mask:0xf bank_mask:0xf
	v_add_f32_dpp v222, v222, v222 row_ror:4 row_mask:0xf bank_mask:0xf
	v_add_f32_dpp v223, v223, v223 row_ror:4 row_mask:0xf bank_mask:0xf
	v_add_f32_dpp v220, v220, v220 row_ror:2 row_mask:0xf bank_mask:0xf
	v_add_f32_dpp v221, v221, v221 row_ror:2 row_mask:0xf bank_mask:0xf
	v_add_f32_dpp v222, v222, v222 row_ror:2 row_mask:0xf bank_mask:0xf
	v_add_f32_dpp v223, v223, v223 row_ror:2 row_mask:0xf bank_mask:0xf
	v_add_f32_dpp v220, v220, v220 row_ror:1 row_mask:0xf bank_mask:0xf
	v_add_f32_dpp v221, v221, v221 row_ror:1 row_mask:0xf bank_mask:0xf
	v_add_f32_dpp v222, v222, v222 row_ror:1 row_mask:0xf bank_mask:0xf
	v_add_f32_dpp v223, v223, v223 row_ror:1 row_mask:0xf bank_mask:0xf
	v_fmamk_f32 v226, v220, 0x3b800000, v7
	v_rsq_f32_e32 v226, v226
	v_lshlrev_b32_e32 v224, 16, v108
	v_lshlrev_b32_e32 v225, 16, v109
	v_mul_f32_e32 v204, v204, v226
	v_mul_f32_e32 v205, v205, v226
	v_mul_f32_e32 v206, v206, v226
	v_mul_f32_e32 v207, v207, v226
	v_mul_f32_e32 v204, v2, v204
	v_mul_f32_e32 v205, v3, v205
	v_mul_f32_e32 v206, v4, v206
	v_mul_f32_e32 v207, v5, v207
	v_and_b32_e32 v108, 0xffff0000, v108
	v_and_b32_e32 v109, 0xffff0000, v109
	v_mul_f32_e32 v226, 0xbfb8aa3b, v224
	v_mul_f32_e32 v227, 0xbfb8aa3b, v108
	v_mul_f32_e32 v1, 0xbfb8aa3b, v225
	v_mul_f32_e32 v220, 0xbfb8aa3b, v109
	v_exp_f32_e32 v226, v226
	v_exp_f32_e32 v227, v227
	v_exp_f32_e32 v1, v1
	v_exp_f32_e32 v220, v220
	v_add_f32_e32 v226, 1.0, v226
	v_add_f32_e32 v227, 1.0, v227
	v_add_f32_e32 v1, 1.0, v1
	v_add_f32_e32 v220, 1.0, v220
	v_rcp_f32_e32 v226, v226
	v_rcp_f32_e32 v227, v227
	v_rcp_f32_e32 v1, v1
	v_rcp_f32_e32 v220, v220
	v_mul_f32_e32 v224, v226, v224
	v_mul_f32_e32 v108, v227, v108
	v_mul_f32_e32 v225, v1, v225
	v_mul_f32_e32 v109, v220, v109
	v_mul_f32_e32 v204, v224, v204
	v_mul_f32_e32 v205, v108, v205
	v_mul_f32_e32 v206, v225, v206
	v_mul_f32_e32 v207, v109, v207
	v_cvt_pk_bf16_f32 v224, v204, v205
	v_cvt_pk_bf16_f32 v225, v206, v207
	s_cmp_gt_i32 s14, 0xffff
	s_cbranch_scc1 .Lgc_skip_b_0
	s_lshr_b32 s17, s14, 2
	s_and_b32 s18, s14, 3
	s_lshl_b32 s17, s17, 12
	s_lshl_b32 s18, s18, 9
	s_add_i32 s17, s17, s18
	v_add_u32_e32 v227, s17, v6
	global_store_dwordx2 v227, v[224:225], s[24:25]
.Lgc_skip_b_0:
	s_add_i32 s14, s14, s9
	v_fmamk_f32 v224, v221, 0x3b800000, v7
	v_rsq_f32_e32 v224, v224
	v_lshlrev_b32_e32 v226, 16, v114
	v_lshlrev_b32_e32 v227, 16, v115
	v_mul_f32_e32 v208, v208, v224
	v_mul_f32_e32 v209, v209, v224
	v_mul_f32_e32 v210, v210, v224
	v_mul_f32_e32 v211, v211, v224
	v_mul_f32_e32 v208, v2, v208
	v_mul_f32_e32 v209, v3, v209
	v_mul_f32_e32 v210, v4, v210
	v_mul_f32_e32 v211, v5, v211
	v_and_b32_e32 v114, 0xffff0000, v114
	v_and_b32_e32 v115, 0xffff0000, v115
	v_mul_f32_e32 v224, 0xbfb8aa3b, v226
	v_mul_f32_e32 v225, 0xbfb8aa3b, v114
	v_mul_f32_e32 v1, 0xbfb8aa3b, v227
	v_mul_f32_e32 v221, 0xbfb8aa3b, v115
	v_exp_f32_e32 v224, v224
	v_exp_f32_e32 v225, v225
	v_exp_f32_e32 v1, v1
	v_exp_f32_e32 v221, v221
	v_add_f32_e32 v224, 1.0, v224
	v_add_f32_e32 v225, 1.0, v225
	v_add_f32_e32 v1, 1.0, v1
	v_add_f32_e32 v221, 1.0, v221
	v_rcp_f32_e32 v224, v224
	v_rcp_f32_e32 v225, v225
	v_rcp_f32_e32 v1, v1
	v_rcp_f32_e32 v221, v221
	v_mul_f32_e32 v226, v224, v226
	v_mul_f32_e32 v114, v225, v114
	v_mul_f32_e32 v227, v1, v227
	v_mul_f32_e32 v115, v221, v115
	v_mul_f32_e32 v208, v226, v208
	v_mul_f32_e32 v209, v114, v209
	v_mul_f32_e32 v210, v227, v210
	v_mul_f32_e32 v211, v115, v211
	v_cvt_pk_bf16_f32 v226, v208, v209
	v_cvt_pk_bf16_f32 v227, v210, v211
	s_cmp_gt_i32 s14, 0xffff
	s_cbranch_scc1 .Lgc_skip_b_1
	s_lshr_b32 s17, s14, 2
	s_and_b32 s18, s14, 3
	s_lshl_b32 s17, s17, 12
	s_lshl_b32 s18, s18, 9
	s_add_i32 s17, s17, s18
	v_add_u32_e32 v225, s17, v6
	global_store_dwordx2 v225, v[226:227], s[24:25]
.Lgc_skip_b_1:
	s_add_i32 s14, s14, s9
	v_fmamk_f32 v226, v222, 0x3b800000, v7
	v_rsq_f32_e32 v226, v226
	v_lshlrev_b32_e32 v224, 16, v120
	v_lshlrev_b32_e32 v225, 16, v121
	v_mul_f32_e32 v212, v212, v226
	v_mul_f32_e32 v213, v213, v226
	v_mul_f32_e32 v214, v214, v226
	v_mul_f32_e32 v215, v215, v226
	v_mul_f32_e32 v212, v2, v212
	v_mul_f32_e32 v213, v3, v213
	v_mul_f32_e32 v214, v4, v214
	v_mul_f32_e32 v215, v5, v215
	v_and_b32_e32 v120, 0xffff0000, v120
	v_and_b32_e32 v121, 0xffff0000, v121
	v_mul_f32_e32 v226, 0xbfb8aa3b, v224
	v_mul_f32_e32 v227, 0xbfb8aa3b, v120
	v_mul_f32_e32 v1, 0xbfb8aa3b, v225
	v_mul_f32_e32 v222, 0xbfb8aa3b, v121
	v_exp_f32_e32 v226, v226
	v_exp_f32_e32 v227, v227
	v_exp_f32_e32 v1, v1
	v_exp_f32_e32 v222, v222
	v_add_f32_e32 v226, 1.0, v226
	v_add_f32_e32 v227, 1.0, v227
	v_add_f32_e32 v1, 1.0, v1
	v_add_f32_e32 v222, 1.0, v222
	v_rcp_f32_e32 v226, v226
	v_rcp_f32_e32 v227, v227
	v_rcp_f32_e32 v1, v1
	v_rcp_f32_e32 v222, v222
	v_mul_f32_e32 v224, v226, v224
	v_mul_f32_e32 v120, v227, v120
	v_mul_f32_e32 v225, v1, v225
	v_mul_f32_e32 v121, v222, v121
	v_mul_f32_e32 v212, v224, v212
	v_mul_f32_e32 v213, v120, v213
	v_mul_f32_e32 v214, v225, v214
	v_mul_f32_e32 v215, v121, v215
	v_cvt_pk_bf16_f32 v224, v212, v213
	v_cvt_pk_bf16_f32 v225, v214, v215
	s_cmp_gt_i32 s14, 0xffff
	s_cbranch_scc1 .Lgc_skip_b_2
	s_lshr_b32 s17, s14, 2
	s_and_b32 s18, s14, 3
	s_lshl_b32 s17, s17, 12
	s_lshl_b32 s18, s18, 9
	s_add_i32 s17, s17, s18
	v_add_u32_e32 v227, s17, v6
	global_store_dwordx2 v227, v[224:225], s[24:25]
.Lgc_skip_b_2:
	s_add_i32 s14, s14, s9
	v_fmamk_f32 v224, v223, 0x3b800000, v7
	v_rsq_f32_e32 v224, v224
	v_lshlrev_b32_e32 v226, 16, v126
	v_lshlrev_b32_e32 v227, 16, v127
	v_mul_f32_e32 v216, v216, v224
	v_mul_f32_e32 v217, v217, v224
	v_mul_f32_e32 v218, v218, v224
	v_mul_f32_e32 v219, v219, v224
	v_mul_f32_e32 v216, v2, v216
	v_mul_f32_e32 v217, v3, v217
	v_mul_f32_e32 v218, v4, v218
	v_mul_f32_e32 v219, v5, v219
	v_and_b32_e32 v126, 0xffff0000, v126
	v_and_b32_e32 v127, 0xffff0000, v127
	v_mul_f32_e32 v224, 0xbfb8aa3b, v226
	v_mul_f32_e32 v225, 0xbfb8aa3b, v126
	v_mul_f32_e32 v1, 0xbfb8aa3b, v227
	v_mul_f32_e32 v223, 0xbfb8aa3b, v127
	v_exp_f32_e32 v224, v224
	v_exp_f32_e32 v225, v225
	v_exp_f32_e32 v1, v1
	v_exp_f32_e32 v223, v223
	v_add_f32_e32 v224, 1.0, v224
	v_add_f32_e32 v225, 1.0, v225
	v_add_f32_e32 v1, 1.0, v1
	v_add_f32_e32 v223, 1.0, v223
	v_rcp_f32_e32 v224, v224
	v_rcp_f32_e32 v225, v225
	v_rcp_f32_e32 v1, v1
	v_rcp_f32_e32 v223, v223
	v_mul_f32_e32 v226, v224, v226
	v_mul_f32_e32 v126, v225, v126
	v_mul_f32_e32 v227, v1, v227
	v_mul_f32_e32 v127, v223, v127
	v_mul_f32_e32 v216, v226, v216
	v_mul_f32_e32 v217, v126, v217
	v_mul_f32_e32 v218, v227, v218
	v_mul_f32_e32 v219, v127, v219
	v_cvt_pk_bf16_f32 v226, v216, v217
	v_cvt_pk_bf16_f32 v227, v218, v219
	s_cmp_gt_i32 s14, 0xffff
	s_cbranch_scc1 .Lgc_skip_b_3
	s_lshr_b32 s17, s14, 2
	s_and_b32 s18, s14, 3
	s_lshl_b32 s17, s17, 12
	s_lshl_b32 s18, s18, 9
	s_add_i32 s17, s17, s18
	v_add_u32_e32 v225, s17, v6
	global_store_dwordx2 v225, v[226:227], s[24:25]
.Lgc_skip_b_3:
	s_add_i32 s14, s14, s9
	v_lshlrev_b32_e32 v204, 16, v128
	v_lshlrev_b32_e32 v224, 16, v130
	v_and_b32_e32 v205, 0xffff0000, v128
	v_and_b32_e32 v225, 0xffff0000, v130
	v_add_f32_e32 v204, v204, v224
	v_add_f32_e32 v205, v205, v225
	v_lshlrev_b32_e32 v206, 16, v129
	v_lshlrev_b32_e32 v224, 16, v131
	v_and_b32_e32 v207, 0xffff0000, v129
	v_and_b32_e32 v225, 0xffff0000, v131
	v_add_f32_e32 v206, v206, v224
	v_add_f32_e32 v207, v207, v225
	v_mul_f32_e32 v224, v204, v204
	v_mul_f32_e32 v225, v205, v205
	v_add_f32_e32 v220, v224, v225
	v_mul_f32_e32 v224, v206, v206
	v_mul_f32_e32 v225, v207, v207
	v_add_f32_e32 v220, v224, v220
	v_add_f32_e32 v220, v225, v220
	v_lshlrev_b32_e32 v208, 16, v134
	v_lshlrev_b32_e32 v226, 16, v136
	v_and_b32_e32 v209, 0xffff0000, v134
	v_and_b32_e32 v227, 0xffff0000, v136
	v_add_f32_e32 v208, v208, v226
	v_add_f32_e32 v209, v209, v227
	v_lshlrev_b32_e32 v210, 16, v135
	v_lshlrev_b32_e32 v226, 16, v137
	v_and_b32_e32 v211, 0xffff0000, v135
	v_and_b32_e32 v227, 0xffff0000, v137
	v_add_f32_e32 v210, v210, v226
	v_add_f32_e32 v211, v211, v227
	v_mul_f32_e32 v226, v208, v208
	v_mul_f32_e32 v227, v209, v209
	v_add_f32_e32 v221, v226, v227
	v_mul_f32_e32 v226, v210, v210
	v_mul_f32_e32 v227, v211, v211
	v_add_f32_e32 v221, v226, v221
	v_add_f32_e32 v221, v227, v221
	v_lshlrev_b32_e32 v212, 16, v140
	v_lshlrev_b32_e32 v224, 16, v142
	v_and_b32_e32 v213, 0xffff0000, v140
	v_and_b32_e32 v225, 0xffff0000, v142
	v_add_f32_e32 v212, v212, v224
	v_add_f32_e32 v213, v213, v225
	v_lshlrev_b32_e32 v214, 16, v141
	v_lshlrev_b32_e32 v224, 16, v143
	v_and_b32_e32 v215, 0xffff0000, v141
	v_and_b32_e32 v225, 0xffff0000, v143
	v_add_f32_e32 v214, v214, v224
	v_add_f32_e32 v215, v215, v225
	v_mul_f32_e32 v224, v212, v212
	v_mul_f32_e32 v225, v213, v213
	v_add_f32_e32 v222, v224, v225
	v_mul_f32_e32 v224, v214, v214
	v_mul_f32_e32 v225, v215, v215
	v_add_f32_e32 v222, v224, v222
	v_add_f32_e32 v222, v225, v222
	v_lshlrev_b32_e32 v216, 16, v146
	v_lshlrev_b32_e32 v226, 16, v148
	v_and_b32_e32 v217, 0xffff0000, v146
	v_and_b32_e32 v227, 0xffff0000, v148
	v_add_f32_e32 v216, v216, v226
	v_add_f32_e32 v217, v217, v227
	v_lshlrev_b32_e32 v218, 16, v147
	v_lshlrev_b32_e32 v226, 16, v149
	v_and_b32_e32 v219, 0xffff0000, v147
	v_and_b32_e32 v227, 0xffff0000, v149
	v_add_f32_e32 v218, v218, v226
	v_add_f32_e32 v219, v219, v227
	v_mul_f32_e32 v226, v216, v216
	v_mul_f32_e32 v227, v217, v217
	v_add_f32_e32 v223, v226, v227
	v_mul_f32_e32 v226, v218, v218
	v_mul_f32_e32 v227, v219, v219
	v_add_f32_e32 v223, v226, v223
	v_add_f32_e32 v223, v227, v223
	v_mov_b32_e32 v224, v220
	v_mov_b32_e32 v225, v221
	v_mov_b32_e32 v226, v222
	v_mov_b32_e32 v227, v223
	v_permlane32_swap_b32_e32 v220, v224
	v_permlane32_swap_b32_e32 v221, v225
	v_permlane32_swap_b32_e32 v222, v226
	v_permlane32_swap_b32_e32 v223, v227
	v_add_f32_e32 v220, v220, v224
	v_add_f32_e32 v221, v221, v225
	v_add_f32_e32 v222, v222, v226
	v_add_f32_e32 v223, v223, v227
	v_mov_b32_e32 v224, v220
	v_mov_b32_e32 v225, v221
	v_mov_b32_e32 v226, v222
	v_mov_b32_e32 v227, v223
	v_permlane16_swap_b32_e32 v220, v224
	v_permlane16_swap_b32_e32 v221, v225
	v_permlane16_swap_b32_e32 v222, v226
	v_permlane16_swap_b32_e32 v223, v227
	v_add_f32_e32 v220, v220, v224
	v_add_f32_e32 v221, v221, v225
	v_add_f32_e32 v222, v222, v226
	v_add_f32_e32 v223, v223, v227
	v_add_f32_dpp v220, v220, v220 row_ror:8 row_mask:0xf bank_mask:0xf
	v_add_f32_dpp v221, v221, v221 row_ror:8 row_mask:0xf bank_mask:0xf
	v_add_f32_dpp v222, v222, v222 row_ror:8 row_mask:0xf bank_mask:0xf
	v_add_f32_dpp v223, v223, v223 row_ror:8 row_mask:0xf bank_mask:0xf
	v_add_f32_dpp v220, v220, v220 row_ror:4 row_mask:0xf bank_mask:0xf
	v_add_f32_dpp v221, v221, v221 row_ror:4 row_mask:0xf bank_mask:0xf
	v_add_f32_dpp v222, v222, v222 row_ror:4 row_mask:0xf bank_mask:0xf
	v_add_f32_dpp v223, v223, v223 row_ror:4 row_mask:0xf bank_mask:0xf
	v_add_f32_dpp v220, v220, v220 row_ror:2 row_mask:0xf bank_mask:0xf
	v_add_f32_dpp v221, v221, v221 row_ror:2 row_mask:0xf bank_mask:0xf
	v_add_f32_dpp v222, v222, v222 row_ror:2 row_mask:0xf bank_mask:0xf
	v_add_f32_dpp v223, v223, v223 row_ror:2 row_mask:0xf bank_mask:0xf
	v_add_f32_dpp v220, v220, v220 row_ror:1 row_mask:0xf bank_mask:0xf
	v_add_f32_dpp v221, v221, v221 row_ror:1 row_mask:0xf bank_mask:0xf
	v_add_f32_dpp v222, v222, v222 row_ror:1 row_mask:0xf bank_mask:0xf
	v_add_f32_dpp v223, v223, v223 row_ror:1 row_mask:0xf bank_mask:0xf
	v_fmamk_f32 v226, v220, 0x3b800000, v7
	v_rsq_f32_e32 v226, v226
	v_lshlrev_b32_e32 v224, 16, v132
	v_lshlrev_b32_e32 v225, 16, v133
	v_mul_f32_e32 v204, v204, v226
	v_mul_f32_e32 v205, v205, v226
	v_mul_f32_e32 v206, v206, v226
	v_mul_f32_e32 v207, v207, v226
	v_mul_f32_e32 v204, v2, v204
	v_mul_f32_e32 v205, v3, v205
	v_mul_f32_e32 v206, v4, v206
	v_mul_f32_e32 v207, v5, v207
	v_and_b32_e32 v132, 0xffff0000, v132
	v_and_b32_e32 v133, 0xffff0000, v133
	v_mul_f32_e32 v226, 0xbfb8aa3b, v224
	v_mul_f32_e32 v227, 0xbfb8aa3b, v132
	v_mul_f32_e32 v1, 0xbfb8aa3b, v225
	v_mul_f32_e32 v220, 0xbfb8aa3b, v133
	v_exp_f32_e32 v226, v226
	v_exp_f32_e32 v227, v227
	v_exp_f32_e32 v1, v1
	v_exp_f32_e32 v220, v220
	v_add_f32_e32 v226, 1.0, v226
	v_add_f32_e32 v227, 1.0, v227
	v_add_f32_e32 v1, 1.0, v1
	v_add_f32_e32 v220, 1.0, v220
	v_rcp_f32_e32 v226, v226
	v_rcp_f32_e32 v227, v227
	v_rcp_f32_e32 v1, v1
	v_rcp_f32_e32 v220, v220
	v_mul_f32_e32 v224, v226, v224
	v_mul_f32_e32 v132, v227, v132
	v_mul_f32_e32 v225, v1, v225
	v_mul_f32_e32 v133, v220, v133
	v_mul_f32_e32 v204, v224, v204
	v_mul_f32_e32 v205, v132, v205
	v_mul_f32_e32 v206, v225, v206
	v_mul_f32_e32 v207, v133, v207
	v_cvt_pk_bf16_f32 v224, v204, v205
	v_cvt_pk_bf16_f32 v225, v206, v207
	s_cmp_gt_i32 s14, 0xffff
	s_cbranch_scc1 .Lgc_skip_b_4
	s_lshr_b32 s17, s14, 2
	s_and_b32 s18, s14, 3
	s_lshl_b32 s17, s17, 12
	s_lshl_b32 s18, s18, 9
	s_add_i32 s17, s17, s18
	v_add_u32_e32 v227, s17, v6
	global_store_dwordx2 v227, v[224:225], s[24:25]
.Lgc_skip_b_4:
	s_add_i32 s14, s14, s9
	v_fmamk_f32 v224, v221, 0x3b800000, v7
	v_rsq_f32_e32 v224, v224
	v_lshlrev_b32_e32 v226, 16, v138
	v_lshlrev_b32_e32 v227, 16, v139
	v_mul_f32_e32 v208, v208, v224
	v_mul_f32_e32 v209, v209, v224
	v_mul_f32_e32 v210, v210, v224
	v_mul_f32_e32 v211, v211, v224
	v_mul_f32_e32 v208, v2, v208
	v_mul_f32_e32 v209, v3, v209
	v_mul_f32_e32 v210, v4, v210
	v_mul_f32_e32 v211, v5, v211
	v_and_b32_e32 v138, 0xffff0000, v138
	v_and_b32_e32 v139, 0xffff0000, v139
	v_mul_f32_e32 v224, 0xbfb8aa3b, v226
	v_mul_f32_e32 v225, 0xbfb8aa3b, v138
	v_mul_f32_e32 v1, 0xbfb8aa3b, v227
	v_mul_f32_e32 v221, 0xbfb8aa3b, v139
	v_exp_f32_e32 v224, v224
	v_exp_f32_e32 v225, v225
	v_exp_f32_e32 v1, v1
	v_exp_f32_e32 v221, v221
	v_add_f32_e32 v224, 1.0, v224
	v_add_f32_e32 v225, 1.0, v225
	v_add_f32_e32 v1, 1.0, v1
	v_add_f32_e32 v221, 1.0, v221
	v_rcp_f32_e32 v224, v224
	v_rcp_f32_e32 v225, v225
	v_rcp_f32_e32 v1, v1
	v_rcp_f32_e32 v221, v221
	v_mul_f32_e32 v226, v224, v226
	v_mul_f32_e32 v138, v225, v138
	v_mul_f32_e32 v227, v1, v227
	v_mul_f32_e32 v139, v221, v139
	v_mul_f32_e32 v208, v226, v208
	v_mul_f32_e32 v209, v138, v209
	v_mul_f32_e32 v210, v227, v210
	v_mul_f32_e32 v211, v139, v211
	v_cvt_pk_bf16_f32 v226, v208, v209
	v_cvt_pk_bf16_f32 v227, v210, v211
	s_cmp_gt_i32 s14, 0xffff
	s_cbranch_scc1 .Lgc_skip_b_5
	s_lshr_b32 s17, s14, 2
	s_and_b32 s18, s14, 3
	s_lshl_b32 s17, s17, 12
	s_lshl_b32 s18, s18, 9
	s_add_i32 s17, s17, s18
	v_add_u32_e32 v225, s17, v6
	global_store_dwordx2 v225, v[226:227], s[24:25]
.Lgc_skip_b_5:
	s_add_i32 s14, s14, s9
	v_fmamk_f32 v226, v222, 0x3b800000, v7
	v_rsq_f32_e32 v226, v226
	v_lshlrev_b32_e32 v224, 16, v144
	v_lshlrev_b32_e32 v225, 16, v145
	v_mul_f32_e32 v212, v212, v226
	v_mul_f32_e32 v213, v213, v226
	v_mul_f32_e32 v214, v214, v226
	v_mul_f32_e32 v215, v215, v226
	v_mul_f32_e32 v212, v2, v212
	v_mul_f32_e32 v213, v3, v213
	v_mul_f32_e32 v214, v4, v214
	v_mul_f32_e32 v215, v5, v215
	v_and_b32_e32 v144, 0xffff0000, v144
	v_and_b32_e32 v145, 0xffff0000, v145
	v_mul_f32_e32 v226, 0xbfb8aa3b, v224
	v_mul_f32_e32 v227, 0xbfb8aa3b, v144
	v_mul_f32_e32 v1, 0xbfb8aa3b, v225
	v_mul_f32_e32 v222, 0xbfb8aa3b, v145
	v_exp_f32_e32 v226, v226
	v_exp_f32_e32 v227, v227
	v_exp_f32_e32 v1, v1
	v_exp_f32_e32 v222, v222
	v_add_f32_e32 v226, 1.0, v226
	v_add_f32_e32 v227, 1.0, v227
	v_add_f32_e32 v1, 1.0, v1
	v_add_f32_e32 v222, 1.0, v222
	v_rcp_f32_e32 v226, v226
	v_rcp_f32_e32 v227, v227
	v_rcp_f32_e32 v1, v1
	v_rcp_f32_e32 v222, v222
	v_mul_f32_e32 v224, v226, v224
	v_mul_f32_e32 v144, v227, v144
	v_mul_f32_e32 v225, v1, v225
	v_mul_f32_e32 v145, v222, v145
	v_mul_f32_e32 v212, v224, v212
	v_mul_f32_e32 v213, v144, v213
	v_mul_f32_e32 v214, v225, v214
	v_mul_f32_e32 v215, v145, v215
	v_cvt_pk_bf16_f32 v224, v212, v213
	v_cvt_pk_bf16_f32 v225, v214, v215
	s_cmp_gt_i32 s14, 0xffff
	s_cbranch_scc1 .Lgc_skip_b_6
	s_lshr_b32 s17, s14, 2
	s_and_b32 s18, s14, 3
	s_lshl_b32 s17, s17, 12
	s_lshl_b32 s18, s18, 9
	s_add_i32 s17, s17, s18
	v_add_u32_e32 v227, s17, v6
	global_store_dwordx2 v227, v[224:225], s[24:25]
.Lgc_skip_b_6:
	s_add_i32 s14, s14, s9
	v_fmamk_f32 v224, v223, 0x3b800000, v7
	v_rsq_f32_e32 v224, v224
	v_lshlrev_b32_e32 v226, 16, v150
	v_lshlrev_b32_e32 v227, 16, v151
	v_mul_f32_e32 v216, v216, v224
	v_mul_f32_e32 v217, v217, v224
	v_mul_f32_e32 v218, v218, v224
	v_mul_f32_e32 v219, v219, v224
	v_mul_f32_e32 v216, v2, v216
	v_mul_f32_e32 v217, v3, v217
	v_mul_f32_e32 v218, v4, v218
	v_mul_f32_e32 v219, v5, v219
	v_and_b32_e32 v150, 0xffff0000, v150
	v_and_b32_e32 v151, 0xffff0000, v151
	v_mul_f32_e32 v224, 0xbfb8aa3b, v226
	v_mul_f32_e32 v225, 0xbfb8aa3b, v150
	v_mul_f32_e32 v1, 0xbfb8aa3b, v227
	v_mul_f32_e32 v223, 0xbfb8aa3b, v151
	v_exp_f32_e32 v224, v224
	v_exp_f32_e32 v225, v225
	v_exp_f32_e32 v1, v1
	v_exp_f32_e32 v223, v223
	v_add_f32_e32 v224, 1.0, v224
	v_add_f32_e32 v225, 1.0, v225
	v_add_f32_e32 v1, 1.0, v1
	v_add_f32_e32 v223, 1.0, v223
	v_rcp_f32_e32 v224, v224
	v_rcp_f32_e32 v225, v225
	v_rcp_f32_e32 v1, v1
	v_rcp_f32_e32 v223, v223
	v_mul_f32_e32 v226, v224, v226
	v_mul_f32_e32 v150, v225, v150
	v_mul_f32_e32 v227, v1, v227
	v_mul_f32_e32 v151, v223, v151
	v_mul_f32_e32 v216, v226, v216
	v_mul_f32_e32 v217, v150, v217
	v_mul_f32_e32 v218, v227, v218
	v_mul_f32_e32 v219, v151, v219
	v_cvt_pk_bf16_f32 v226, v216, v217
	v_cvt_pk_bf16_f32 v227, v218, v219
	s_cmp_gt_i32 s14, 0xffff
	s_cbranch_scc1 .Lgc_skip_b_7
	s_lshr_b32 s17, s14, 2
	s_and_b32 s18, s14, 3
	s_lshl_b32 s17, s17, 12
	s_lshl_b32 s18, s18, 9
	s_add_i32 s17, s17, s18
	v_add_u32_e32 v225, s17, v6
	global_store_dwordx2 v225, v[226:227], s[24:25]
.Lgc_skip_b_7:
	s_add_i32 s14, s14, s9
	v_lshlrev_b32_e32 v204, 16, v152
	v_lshlrev_b32_e32 v224, 16, v154
	v_and_b32_e32 v205, 0xffff0000, v152
	v_and_b32_e32 v225, 0xffff0000, v154
	v_add_f32_e32 v204, v204, v224
	v_add_f32_e32 v205, v205, v225
	v_lshlrev_b32_e32 v206, 16, v153
	v_lshlrev_b32_e32 v224, 16, v155
	v_and_b32_e32 v207, 0xffff0000, v153
	v_and_b32_e32 v225, 0xffff0000, v155
	v_add_f32_e32 v206, v206, v224
	v_add_f32_e32 v207, v207, v225
	v_mul_f32_e32 v224, v204, v204
	v_mul_f32_e32 v225, v205, v205
	v_add_f32_e32 v220, v224, v225
	v_mul_f32_e32 v224, v206, v206
	v_mul_f32_e32 v225, v207, v207
	v_add_f32_e32 v220, v224, v220
	v_add_f32_e32 v220, v225, v220
	v_lshlrev_b32_e32 v208, 16, v158
	v_lshlrev_b32_e32 v226, 16, v160
	v_and_b32_e32 v209, 0xffff0000, v158
	v_and_b32_e32 v227, 0xffff0000, v160
	v_add_f32_e32 v208, v208, v226
	v_add_f32_e32 v209, v209, v227
	v_lshlrev_b32_e32 v210, 16, v159
	v_lshlrev_b32_e32 v226, 16, v161
	v_and_b32_e32 v211, 0xffff0000, v159
	v_and_b32_e32 v227, 0xffff0000, v161
	v_add_f32_e32 v210, v210, v226
	v_add_f32_e32 v211, v211, v227
	v_mul_f32_e32 v226, v208, v208
	v_mul_f32_e32 v227, v209, v209
	v_add_f32_e32 v221, v226, v227
	v_mul_f32_e32 v226, v210, v210
	v_mul_f32_e32 v227, v211, v211
	v_add_f32_e32 v221, v226, v221
	v_add_f32_e32 v221, v227, v221
	v_lshlrev_b32_e32 v212, 16, v164
	v_lshlrev_b32_e32 v224, 16, v166
	v_and_b32_e32 v213, 0xffff0000, v164
	v_and_b32_e32 v225, 0xffff0000, v166
	v_add_f32_e32 v212, v212, v224
	v_add_f32_e32 v213, v213, v225
	v_lshlrev_b32_e32 v214, 16, v165
	v_lshlrev_b32_e32 v224, 16, v167
	v_and_b32_e32 v215, 0xffff0000, v165
	v_and_b32_e32 v225, 0xffff0000, v167
	v_add_f32_e32 v214, v214, v224
	v_add_f32_e32 v215, v215, v225
	v_mul_f32_e32 v224, v212, v212
	v_mul_f32_e32 v225, v213, v213
	v_add_f32_e32 v222, v224, v225
	v_mul_f32_e32 v224, v214, v214
	v_mul_f32_e32 v225, v215, v215
	v_add_f32_e32 v222, v224, v222
	v_add_f32_e32 v222, v225, v222
	v_lshlrev_b32_e32 v216, 16, v170
	v_lshlrev_b32_e32 v226, 16, v172
	v_and_b32_e32 v217, 0xffff0000, v170
	v_and_b32_e32 v227, 0xffff0000, v172
	v_add_f32_e32 v216, v216, v226
	v_add_f32_e32 v217, v217, v227
	v_lshlrev_b32_e32 v218, 16, v171
	v_lshlrev_b32_e32 v226, 16, v173
	v_and_b32_e32 v219, 0xffff0000, v171
	v_and_b32_e32 v227, 0xffff0000, v173
	v_add_f32_e32 v218, v218, v226
	v_add_f32_e32 v219, v219, v227
	v_mul_f32_e32 v226, v216, v216
	v_mul_f32_e32 v227, v217, v217
	v_add_f32_e32 v223, v226, v227
	v_mul_f32_e32 v226, v218, v218
	v_mul_f32_e32 v227, v219, v219
	v_add_f32_e32 v223, v226, v223
	v_add_f32_e32 v223, v227, v223
	v_mov_b32_e32 v224, v220
	v_mov_b32_e32 v225, v221
	v_mov_b32_e32 v226, v222
	v_mov_b32_e32 v227, v223
	v_permlane32_swap_b32_e32 v220, v224
	v_permlane32_swap_b32_e32 v221, v225
	v_permlane32_swap_b32_e32 v222, v226
	v_permlane32_swap_b32_e32 v223, v227
	v_add_f32_e32 v220, v220, v224
	v_add_f32_e32 v221, v221, v225
	v_add_f32_e32 v222, v222, v226
	v_add_f32_e32 v223, v223, v227
	v_mov_b32_e32 v224, v220
	v_mov_b32_e32 v225, v221
	v_mov_b32_e32 v226, v222
	v_mov_b32_e32 v227, v223
	v_permlane16_swap_b32_e32 v220, v224
	v_permlane16_swap_b32_e32 v221, v225
	v_permlane16_swap_b32_e32 v222, v226
	v_permlane16_swap_b32_e32 v223, v227
	v_add_f32_e32 v220, v220, v224
	v_add_f32_e32 v221, v221, v225
	v_add_f32_e32 v222, v222, v226
	v_add_f32_e32 v223, v223, v227
	v_add_f32_dpp v220, v220, v220 row_ror:8 row_mask:0xf bank_mask:0xf
	v_add_f32_dpp v221, v221, v221 row_ror:8 row_mask:0xf bank_mask:0xf
	v_add_f32_dpp v222, v222, v222 row_ror:8 row_mask:0xf bank_mask:0xf
	v_add_f32_dpp v223, v223, v223 row_ror:8 row_mask:0xf bank_mask:0xf
	v_add_f32_dpp v220, v220, v220 row_ror:4 row_mask:0xf bank_mask:0xf
	v_add_f32_dpp v221, v221, v221 row_ror:4 row_mask:0xf bank_mask:0xf
	v_add_f32_dpp v222, v222, v222 row_ror:4 row_mask:0xf bank_mask:0xf
	v_add_f32_dpp v223, v223, v223 row_ror:4 row_mask:0xf bank_mask:0xf
	v_add_f32_dpp v220, v220, v220 row_ror:2 row_mask:0xf bank_mask:0xf
	v_add_f32_dpp v221, v221, v221 row_ror:2 row_mask:0xf bank_mask:0xf
	v_add_f32_dpp v222, v222, v222 row_ror:2 row_mask:0xf bank_mask:0xf
	v_add_f32_dpp v223, v223, v223 row_ror:2 row_mask:0xf bank_mask:0xf
	v_add_f32_dpp v220, v220, v220 row_ror:1 row_mask:0xf bank_mask:0xf
	v_add_f32_dpp v221, v221, v221 row_ror:1 row_mask:0xf bank_mask:0xf
	v_add_f32_dpp v222, v222, v222 row_ror:1 row_mask:0xf bank_mask:0xf
	v_add_f32_dpp v223, v223, v223 row_ror:1 row_mask:0xf bank_mask:0xf
	v_fmamk_f32 v226, v220, 0x3b800000, v7
	v_rsq_f32_e32 v226, v226
	v_lshlrev_b32_e32 v224, 16, v156
	v_lshlrev_b32_e32 v225, 16, v157
	v_mul_f32_e32 v204, v204, v226
	v_mul_f32_e32 v205, v205, v226
	v_mul_f32_e32 v206, v206, v226
	v_mul_f32_e32 v207, v207, v226
	v_mul_f32_e32 v204, v2, v204
	v_mul_f32_e32 v205, v3, v205
	v_mul_f32_e32 v206, v4, v206
	v_mul_f32_e32 v207, v5, v207
	v_and_b32_e32 v156, 0xffff0000, v156
	v_and_b32_e32 v157, 0xffff0000, v157
	v_mul_f32_e32 v226, 0xbfb8aa3b, v224
	v_mul_f32_e32 v227, 0xbfb8aa3b, v156
	v_mul_f32_e32 v1, 0xbfb8aa3b, v225
	v_mul_f32_e32 v220, 0xbfb8aa3b, v157
	v_exp_f32_e32 v226, v226
	v_exp_f32_e32 v227, v227
	v_exp_f32_e32 v1, v1
	v_exp_f32_e32 v220, v220
	v_add_f32_e32 v226, 1.0, v226
	v_add_f32_e32 v227, 1.0, v227
	v_add_f32_e32 v1, 1.0, v1
	v_add_f32_e32 v220, 1.0, v220
	v_rcp_f32_e32 v226, v226
	v_rcp_f32_e32 v227, v227
	v_rcp_f32_e32 v1, v1
	v_rcp_f32_e32 v220, v220
	v_mul_f32_e32 v224, v226, v224
	v_mul_f32_e32 v156, v227, v156
	v_mul_f32_e32 v225, v1, v225
	v_mul_f32_e32 v157, v220, v157
	v_mul_f32_e32 v204, v224, v204
	v_mul_f32_e32 v205, v156, v205
	v_mul_f32_e32 v206, v225, v206
	v_mul_f32_e32 v207, v157, v207
	v_cvt_pk_bf16_f32 v224, v204, v205
	v_cvt_pk_bf16_f32 v225, v206, v207
	s_cmp_gt_i32 s14, 0xffff
	s_cbranch_scc1 .Lgc_skip_b_8
	s_lshr_b32 s17, s14, 2
	s_and_b32 s18, s14, 3
	s_lshl_b32 s17, s17, 12
	s_lshl_b32 s18, s18, 9
	s_add_i32 s17, s17, s18
	v_add_u32_e32 v227, s17, v6
	global_store_dwordx2 v227, v[224:225], s[24:25]
.Lgc_skip_b_8:
	s_add_i32 s14, s14, s9
	v_fmamk_f32 v224, v221, 0x3b800000, v7
	v_rsq_f32_e32 v224, v224
	v_lshlrev_b32_e32 v226, 16, v162
	v_lshlrev_b32_e32 v227, 16, v163
	v_mul_f32_e32 v208, v208, v224
	v_mul_f32_e32 v209, v209, v224
	v_mul_f32_e32 v210, v210, v224
	v_mul_f32_e32 v211, v211, v224
	v_mul_f32_e32 v208, v2, v208
	v_mul_f32_e32 v209, v3, v209
	v_mul_f32_e32 v210, v4, v210
	v_mul_f32_e32 v211, v5, v211
	v_and_b32_e32 v162, 0xffff0000, v162
	v_and_b32_e32 v163, 0xffff0000, v163
	v_mul_f32_e32 v224, 0xbfb8aa3b, v226
	v_mul_f32_e32 v225, 0xbfb8aa3b, v162
	v_mul_f32_e32 v1, 0xbfb8aa3b, v227
	v_mul_f32_e32 v221, 0xbfb8aa3b, v163
	v_exp_f32_e32 v224, v224
	v_exp_f32_e32 v225, v225
	v_exp_f32_e32 v1, v1
	v_exp_f32_e32 v221, v221
	v_add_f32_e32 v224, 1.0, v224
	v_add_f32_e32 v225, 1.0, v225
	v_add_f32_e32 v1, 1.0, v1
	v_add_f32_e32 v221, 1.0, v221
	v_rcp_f32_e32 v224, v224
	v_rcp_f32_e32 v225, v225
	v_rcp_f32_e32 v1, v1
	v_rcp_f32_e32 v221, v221
	v_mul_f32_e32 v226, v224, v226
	v_mul_f32_e32 v162, v225, v162
	v_mul_f32_e32 v227, v1, v227
	v_mul_f32_e32 v163, v221, v163
	v_mul_f32_e32 v208, v226, v208
	v_mul_f32_e32 v209, v162, v209
	v_mul_f32_e32 v210, v227, v210
	v_mul_f32_e32 v211, v163, v211
	v_cvt_pk_bf16_f32 v226, v208, v209
	v_cvt_pk_bf16_f32 v227, v210, v211
	s_cmp_gt_i32 s14, 0xffff
	s_cbranch_scc1 .Lgc_skip_b_9
	s_lshr_b32 s17, s14, 2
	s_and_b32 s18, s14, 3
	s_lshl_b32 s17, s17, 12
	s_lshl_b32 s18, s18, 9
	s_add_i32 s17, s17, s18
	v_add_u32_e32 v225, s17, v6
	global_store_dwordx2 v225, v[226:227], s[24:25]
.Lgc_skip_b_9:
	s_add_i32 s14, s14, s9
	v_fmamk_f32 v226, v222, 0x3b800000, v7
	v_rsq_f32_e32 v226, v226
	v_lshlrev_b32_e32 v224, 16, v168
	v_lshlrev_b32_e32 v225, 16, v169
	v_mul_f32_e32 v212, v212, v226
	v_mul_f32_e32 v213, v213, v226
	v_mul_f32_e32 v214, v214, v226
	v_mul_f32_e32 v215, v215, v226
	v_mul_f32_e32 v212, v2, v212
	v_mul_f32_e32 v213, v3, v213
	v_mul_f32_e32 v214, v4, v214
	v_mul_f32_e32 v215, v5, v215
	v_and_b32_e32 v168, 0xffff0000, v168
	v_and_b32_e32 v169, 0xffff0000, v169
	v_mul_f32_e32 v226, 0xbfb8aa3b, v224
	v_mul_f32_e32 v227, 0xbfb8aa3b, v168
	v_mul_f32_e32 v1, 0xbfb8aa3b, v225
	v_mul_f32_e32 v222, 0xbfb8aa3b, v169
	v_exp_f32_e32 v226, v226
	v_exp_f32_e32 v227, v227
	v_exp_f32_e32 v1, v1
	v_exp_f32_e32 v222, v222
	v_add_f32_e32 v226, 1.0, v226
	v_add_f32_e32 v227, 1.0, v227
	v_add_f32_e32 v1, 1.0, v1
	v_add_f32_e32 v222, 1.0, v222
	v_rcp_f32_e32 v226, v226
	v_rcp_f32_e32 v227, v227
	v_rcp_f32_e32 v1, v1
	v_rcp_f32_e32 v222, v222
	v_mul_f32_e32 v224, v226, v224
	v_mul_f32_e32 v168, v227, v168
	v_mul_f32_e32 v225, v1, v225
	v_mul_f32_e32 v169, v222, v169
	v_mul_f32_e32 v212, v224, v212
	v_mul_f32_e32 v213, v168, v213
	v_mul_f32_e32 v214, v225, v214
	v_mul_f32_e32 v215, v169, v215
	v_cvt_pk_bf16_f32 v224, v212, v213
	v_cvt_pk_bf16_f32 v225, v214, v215
	s_cmp_gt_i32 s14, 0xffff
	s_cbranch_scc1 .Lgc_skip_b_10
	s_lshr_b32 s17, s14, 2
	s_and_b32 s18, s14, 3
	s_lshl_b32 s17, s17, 12
	s_lshl_b32 s18, s18, 9
	s_add_i32 s17, s17, s18
	v_add_u32_e32 v227, s17, v6
	global_store_dwordx2 v227, v[224:225], s[24:25]
.Lgc_skip_b_10:
	s_add_i32 s14, s14, s9
	v_fmamk_f32 v224, v223, 0x3b800000, v7
	v_rsq_f32_e32 v224, v224
	v_lshlrev_b32_e32 v226, 16, v174
	v_lshlrev_b32_e32 v227, 16, v175
	v_mul_f32_e32 v216, v216, v224
	v_mul_f32_e32 v217, v217, v224
	v_mul_f32_e32 v218, v218, v224
	v_mul_f32_e32 v219, v219, v224
	v_mul_f32_e32 v216, v2, v216
	v_mul_f32_e32 v217, v3, v217
	v_mul_f32_e32 v218, v4, v218
	v_mul_f32_e32 v219, v5, v219
	v_and_b32_e32 v174, 0xffff0000, v174
	v_and_b32_e32 v175, 0xffff0000, v175
	v_mul_f32_e32 v224, 0xbfb8aa3b, v226
	v_mul_f32_e32 v225, 0xbfb8aa3b, v174
	v_mul_f32_e32 v1, 0xbfb8aa3b, v227
	v_mul_f32_e32 v223, 0xbfb8aa3b, v175
	v_exp_f32_e32 v224, v224
	v_exp_f32_e32 v225, v225
	v_exp_f32_e32 v1, v1
	v_exp_f32_e32 v223, v223
	v_add_f32_e32 v224, 1.0, v224
	v_add_f32_e32 v225, 1.0, v225
	v_add_f32_e32 v1, 1.0, v1
	v_add_f32_e32 v223, 1.0, v223
	v_rcp_f32_e32 v224, v224
	v_rcp_f32_e32 v225, v225
	v_rcp_f32_e32 v1, v1
	v_rcp_f32_e32 v223, v223
	v_mul_f32_e32 v226, v224, v226
	v_mul_f32_e32 v174, v225, v174
	v_mul_f32_e32 v227, v1, v227
	v_mul_f32_e32 v175, v223, v175
	v_mul_f32_e32 v216, v226, v216
	v_mul_f32_e32 v217, v174, v217
	v_mul_f32_e32 v218, v227, v218
	v_mul_f32_e32 v219, v175, v219
	v_cvt_pk_bf16_f32 v226, v216, v217
	v_cvt_pk_bf16_f32 v227, v218, v219
	s_cmp_gt_i32 s14, 0xffff
	s_cbranch_scc1 .Lgc_skip_b_11
	s_lshr_b32 s17, s14, 2
	s_and_b32 s18, s14, 3
	s_lshl_b32 s17, s17, 12
	s_lshl_b32 s18, s18, 9
	s_add_i32 s17, s17, s18
	v_add_u32_e32 v225, s17, v6
	global_store_dwordx2 v225, v[226:227], s[24:25]
.Lgc_skip_b_11:
	s_add_i32 s14, s14, s9
	v_lshlrev_b32_e32 v204, 16, v176
	v_lshlrev_b32_e32 v224, 16, v178
	v_and_b32_e32 v205, 0xffff0000, v176
	v_and_b32_e32 v225, 0xffff0000, v178
	v_add_f32_e32 v204, v204, v224
	v_add_f32_e32 v205, v205, v225
	v_lshlrev_b32_e32 v206, 16, v177
	v_lshlrev_b32_e32 v224, 16, v179
	v_and_b32_e32 v207, 0xffff0000, v177
	v_and_b32_e32 v225, 0xffff0000, v179
	v_add_f32_e32 v206, v206, v224
	v_add_f32_e32 v207, v207, v225
	v_mul_f32_e32 v224, v204, v204
	v_mul_f32_e32 v225, v205, v205
	v_add_f32_e32 v220, v224, v225
	v_mul_f32_e32 v224, v206, v206
	v_mul_f32_e32 v225, v207, v207
	v_add_f32_e32 v220, v224, v220
	v_add_f32_e32 v220, v225, v220
	v_lshlrev_b32_e32 v208, 16, v182
	v_lshlrev_b32_e32 v226, 16, v184
	v_and_b32_e32 v209, 0xffff0000, v182
	v_and_b32_e32 v227, 0xffff0000, v184
	v_add_f32_e32 v208, v208, v226
	v_add_f32_e32 v209, v209, v227
	v_lshlrev_b32_e32 v210, 16, v183
	v_lshlrev_b32_e32 v226, 16, v185
	v_and_b32_e32 v211, 0xffff0000, v183
	v_and_b32_e32 v227, 0xffff0000, v185
	v_add_f32_e32 v210, v210, v226
	v_add_f32_e32 v211, v211, v227
	v_mul_f32_e32 v226, v208, v208
	v_mul_f32_e32 v227, v209, v209
	v_add_f32_e32 v221, v226, v227
	v_mul_f32_e32 v226, v210, v210
	v_mul_f32_e32 v227, v211, v211
	v_add_f32_e32 v221, v226, v221
	v_add_f32_e32 v221, v227, v221
	v_lshlrev_b32_e32 v212, 16, v188
	v_lshlrev_b32_e32 v224, 16, v190
	v_and_b32_e32 v213, 0xffff0000, v188
	v_and_b32_e32 v225, 0xffff0000, v190
	v_add_f32_e32 v212, v212, v224
	v_add_f32_e32 v213, v213, v225
	v_lshlrev_b32_e32 v214, 16, v189
	v_lshlrev_b32_e32 v224, 16, v191
	v_and_b32_e32 v215, 0xffff0000, v189
	v_and_b32_e32 v225, 0xffff0000, v191
	v_add_f32_e32 v214, v214, v224
	v_add_f32_e32 v215, v215, v225
	v_mul_f32_e32 v224, v212, v212
	v_mul_f32_e32 v225, v213, v213
	v_add_f32_e32 v222, v224, v225
	v_mul_f32_e32 v224, v214, v214
	v_mul_f32_e32 v225, v215, v215
	v_add_f32_e32 v222, v224, v222
	v_add_f32_e32 v222, v225, v222
	v_lshlrev_b32_e32 v216, 16, v198
	v_lshlrev_b32_e32 v226, 16, v200
	v_and_b32_e32 v217, 0xffff0000, v198
	v_and_b32_e32 v227, 0xffff0000, v200
	v_add_f32_e32 v216, v216, v226
	v_add_f32_e32 v217, v217, v227
	v_lshlrev_b32_e32 v218, 16, v199
	v_lshlrev_b32_e32 v226, 16, v201
	v_and_b32_e32 v219, 0xffff0000, v199
	v_and_b32_e32 v227, 0xffff0000, v201
	v_add_f32_e32 v218, v218, v226
	v_add_f32_e32 v219, v219, v227
	v_mul_f32_e32 v226, v216, v216
	v_mul_f32_e32 v227, v217, v217
	v_add_f32_e32 v223, v226, v227
	v_mul_f32_e32 v226, v218, v218
	v_mul_f32_e32 v227, v219, v219
	v_add_f32_e32 v223, v226, v223
	v_add_f32_e32 v223, v227, v223
	v_mov_b32_e32 v224, v220
	v_mov_b32_e32 v225, v221
	v_mov_b32_e32 v226, v222
	v_mov_b32_e32 v227, v223
	v_permlane32_swap_b32_e32 v220, v224
	v_permlane32_swap_b32_e32 v221, v225
	v_permlane32_swap_b32_e32 v222, v226
	v_permlane32_swap_b32_e32 v223, v227
	v_add_f32_e32 v220, v220, v224
	v_add_f32_e32 v221, v221, v225
	v_add_f32_e32 v222, v222, v226
	v_add_f32_e32 v223, v223, v227
	v_mov_b32_e32 v224, v220
	v_mov_b32_e32 v225, v221
	v_mov_b32_e32 v226, v222
	v_mov_b32_e32 v227, v223
	v_permlane16_swap_b32_e32 v220, v224
	v_permlane16_swap_b32_e32 v221, v225
	v_permlane16_swap_b32_e32 v222, v226
	v_permlane16_swap_b32_e32 v223, v227
	v_add_f32_e32 v220, v220, v224
	v_add_f32_e32 v221, v221, v225
	v_add_f32_e32 v222, v222, v226
	v_add_f32_e32 v223, v223, v227
	v_add_f32_dpp v220, v220, v220 row_ror:8 row_mask:0xf bank_mask:0xf
	v_add_f32_dpp v221, v221, v221 row_ror:8 row_mask:0xf bank_mask:0xf
	v_add_f32_dpp v222, v222, v222 row_ror:8 row_mask:0xf bank_mask:0xf
	v_add_f32_dpp v223, v223, v223 row_ror:8 row_mask:0xf bank_mask:0xf
	v_add_f32_dpp v220, v220, v220 row_ror:4 row_mask:0xf bank_mask:0xf
	v_add_f32_dpp v221, v221, v221 row_ror:4 row_mask:0xf bank_mask:0xf
	v_add_f32_dpp v222, v222, v222 row_ror:4 row_mask:0xf bank_mask:0xf
	v_add_f32_dpp v223, v223, v223 row_ror:4 row_mask:0xf bank_mask:0xf
	v_add_f32_dpp v220, v220, v220 row_ror:2 row_mask:0xf bank_mask:0xf
	v_add_f32_dpp v221, v221, v221 row_ror:2 row_mask:0xf bank_mask:0xf
	v_add_f32_dpp v222, v222, v222 row_ror:2 row_mask:0xf bank_mask:0xf
	v_add_f32_dpp v223, v223, v223 row_ror:2 row_mask:0xf bank_mask:0xf
	v_add_f32_dpp v220, v220, v220 row_ror:1 row_mask:0xf bank_mask:0xf
	v_add_f32_dpp v221, v221, v221 row_ror:1 row_mask:0xf bank_mask:0xf
	v_add_f32_dpp v222, v222, v222 row_ror:1 row_mask:0xf bank_mask:0xf
	v_add_f32_dpp v223, v223, v223 row_ror:1 row_mask:0xf bank_mask:0xf
	v_fmamk_f32 v226, v220, 0x3b800000, v7
	v_rsq_f32_e32 v226, v226
	v_lshlrev_b32_e32 v224, 16, v180
	v_lshlrev_b32_e32 v225, 16, v181
	v_mul_f32_e32 v204, v204, v226
	v_mul_f32_e32 v205, v205, v226
	v_mul_f32_e32 v206, v206, v226
	v_mul_f32_e32 v207, v207, v226
	v_mul_f32_e32 v204, v2, v204
	v_mul_f32_e32 v205, v3, v205
	v_mul_f32_e32 v206, v4, v206
	v_mul_f32_e32 v207, v5, v207
	v_and_b32_e32 v180, 0xffff0000, v180
	v_and_b32_e32 v181, 0xffff0000, v181
	v_mul_f32_e32 v226, 0xbfb8aa3b, v224
	v_mul_f32_e32 v227, 0xbfb8aa3b, v180
	v_mul_f32_e32 v1, 0xbfb8aa3b, v225
	v_mul_f32_e32 v220, 0xbfb8aa3b, v181
	v_exp_f32_e32 v226, v226
	v_exp_f32_e32 v227, v227
	v_exp_f32_e32 v1, v1
	v_exp_f32_e32 v220, v220
	v_add_f32_e32 v226, 1.0, v226
	v_add_f32_e32 v227, 1.0, v227
	v_add_f32_e32 v1, 1.0, v1
	v_add_f32_e32 v220, 1.0, v220
	v_rcp_f32_e32 v226, v226
	v_rcp_f32_e32 v227, v227
	v_rcp_f32_e32 v1, v1
	v_rcp_f32_e32 v220, v220
	v_mul_f32_e32 v224, v226, v224
	v_mul_f32_e32 v180, v227, v180
	v_mul_f32_e32 v225, v1, v225
	v_mul_f32_e32 v181, v220, v181
	v_mul_f32_e32 v204, v224, v204
	v_mul_f32_e32 v205, v180, v205
	v_mul_f32_e32 v206, v225, v206
	v_mul_f32_e32 v207, v181, v207
	v_cvt_pk_bf16_f32 v224, v204, v205
	v_cvt_pk_bf16_f32 v225, v206, v207
	s_cmp_gt_i32 s14, 0xffff
	s_cbranch_scc1 .Lgc_skip_b_12
	s_lshr_b32 s17, s14, 2
	s_and_b32 s18, s14, 3
	s_lshl_b32 s17, s17, 12
	s_lshl_b32 s18, s18, 9
	s_add_i32 s17, s17, s18
	v_add_u32_e32 v227, s17, v6
	global_store_dwordx2 v227, v[224:225], s[24:25]
.Lgc_skip_b_12:
	s_add_i32 s14, s14, s9
	v_fmamk_f32 v224, v221, 0x3b800000, v7
	v_rsq_f32_e32 v224, v224
	v_lshlrev_b32_e32 v226, 16, v186
	v_lshlrev_b32_e32 v227, 16, v187
	v_mul_f32_e32 v208, v208, v224
	v_mul_f32_e32 v209, v209, v224
	v_mul_f32_e32 v210, v210, v224
	v_mul_f32_e32 v211, v211, v224
	v_mul_f32_e32 v208, v2, v208
	v_mul_f32_e32 v209, v3, v209
	v_mul_f32_e32 v210, v4, v210
	v_mul_f32_e32 v211, v5, v211
	v_and_b32_e32 v186, 0xffff0000, v186
	v_and_b32_e32 v187, 0xffff0000, v187
	v_mul_f32_e32 v224, 0xbfb8aa3b, v226
	v_mul_f32_e32 v225, 0xbfb8aa3b, v186
	v_mul_f32_e32 v1, 0xbfb8aa3b, v227
	v_mul_f32_e32 v221, 0xbfb8aa3b, v187
	v_exp_f32_e32 v224, v224
	v_exp_f32_e32 v225, v225
	v_exp_f32_e32 v1, v1
	v_exp_f32_e32 v221, v221
	v_add_f32_e32 v224, 1.0, v224
	v_add_f32_e32 v225, 1.0, v225
	v_add_f32_e32 v1, 1.0, v1
	v_add_f32_e32 v221, 1.0, v221
	v_rcp_f32_e32 v224, v224
	v_rcp_f32_e32 v225, v225
	v_rcp_f32_e32 v1, v1
	v_rcp_f32_e32 v221, v221
	v_mul_f32_e32 v226, v224, v226
	v_mul_f32_e32 v186, v225, v186
	v_mul_f32_e32 v227, v1, v227
	v_mul_f32_e32 v187, v221, v187
	v_mul_f32_e32 v208, v226, v208
	v_mul_f32_e32 v209, v186, v209
	v_mul_f32_e32 v210, v227, v210
	v_mul_f32_e32 v211, v187, v211
	v_cvt_pk_bf16_f32 v226, v208, v209
	v_cvt_pk_bf16_f32 v227, v210, v211
	s_cmp_gt_i32 s14, 0xffff
	s_cbranch_scc1 .Lgc_skip_b_13
	s_lshr_b32 s17, s14, 2
	s_and_b32 s18, s14, 3
	s_lshl_b32 s17, s17, 12
	s_lshl_b32 s18, s18, 9
	s_add_i32 s17, s17, s18
	v_add_u32_e32 v225, s17, v6
	global_store_dwordx2 v225, v[226:227], s[24:25]
.Lgc_skip_b_13:
	s_add_i32 s14, s14, s9
	v_fmamk_f32 v226, v222, 0x3b800000, v7
	v_rsq_f32_e32 v226, v226
	v_lshlrev_b32_e32 v224, 16, v192
	v_lshlrev_b32_e32 v225, 16, v193
	v_mul_f32_e32 v212, v212, v226
	v_mul_f32_e32 v213, v213, v226
	v_mul_f32_e32 v214, v214, v226
	v_mul_f32_e32 v215, v215, v226
	v_mul_f32_e32 v212, v2, v212
	v_mul_f32_e32 v213, v3, v213
	v_mul_f32_e32 v214, v4, v214
	v_mul_f32_e32 v215, v5, v215
	v_and_b32_e32 v192, 0xffff0000, v192
	v_and_b32_e32 v193, 0xffff0000, v193
	v_mul_f32_e32 v226, 0xbfb8aa3b, v224
	v_mul_f32_e32 v227, 0xbfb8aa3b, v192
	v_mul_f32_e32 v1, 0xbfb8aa3b, v225
	v_mul_f32_e32 v222, 0xbfb8aa3b, v193
	v_exp_f32_e32 v226, v226
	v_exp_f32_e32 v227, v227
	v_exp_f32_e32 v1, v1
	v_exp_f32_e32 v222, v222
	v_add_f32_e32 v226, 1.0, v226
	v_add_f32_e32 v227, 1.0, v227
	v_add_f32_e32 v1, 1.0, v1
	v_add_f32_e32 v222, 1.0, v222
	v_rcp_f32_e32 v226, v226
	v_rcp_f32_e32 v227, v227
	v_rcp_f32_e32 v1, v1
	v_rcp_f32_e32 v222, v222
	v_mul_f32_e32 v224, v226, v224
	v_mul_f32_e32 v192, v227, v192
	v_mul_f32_e32 v225, v1, v225
	v_mul_f32_e32 v193, v222, v193
	v_mul_f32_e32 v212, v224, v212
	v_mul_f32_e32 v213, v192, v213
	v_mul_f32_e32 v214, v225, v214
	v_mul_f32_e32 v215, v193, v215
	v_cvt_pk_bf16_f32 v224, v212, v213
	v_cvt_pk_bf16_f32 v225, v214, v215
	s_cmp_gt_i32 s14, 0xffff
	s_cbranch_scc1 .Lgc_skip_b_14
	s_lshr_b32 s17, s14, 2
	s_and_b32 s18, s14, 3
	s_lshl_b32 s17, s17, 12
	s_lshl_b32 s18, s18, 9
	s_add_i32 s17, s17, s18
	v_add_u32_e32 v227, s17, v6
	global_store_dwordx2 v227, v[224:225], s[24:25]
.Lgc_skip_b_14:
	s_add_i32 s14, s14, s9
	v_fmamk_f32 v224, v223, 0x3b800000, v7
	v_rsq_f32_e32 v224, v224
	v_lshlrev_b32_e32 v226, 16, v202
	v_lshlrev_b32_e32 v227, 16, v203
	v_mul_f32_e32 v216, v216, v224
	v_mul_f32_e32 v217, v217, v224
	v_mul_f32_e32 v218, v218, v224
	v_mul_f32_e32 v219, v219, v224
	v_mul_f32_e32 v216, v2, v216
	v_mul_f32_e32 v217, v3, v217
	v_mul_f32_e32 v218, v4, v218
	v_mul_f32_e32 v219, v5, v219
	v_and_b32_e32 v202, 0xffff0000, v202
	v_and_b32_e32 v203, 0xffff0000, v203
	v_mul_f32_e32 v224, 0xbfb8aa3b, v226
	v_mul_f32_e32 v225, 0xbfb8aa3b, v202
	v_mul_f32_e32 v1, 0xbfb8aa3b, v227
	v_mul_f32_e32 v223, 0xbfb8aa3b, v203
	v_exp_f32_e32 v224, v224
	v_exp_f32_e32 v225, v225
	v_exp_f32_e32 v1, v1
	v_exp_f32_e32 v223, v223
	v_add_f32_e32 v224, 1.0, v224
	v_add_f32_e32 v225, 1.0, v225
	v_add_f32_e32 v1, 1.0, v1
	v_add_f32_e32 v223, 1.0, v223
	v_rcp_f32_e32 v224, v224
	v_rcp_f32_e32 v225, v225
	v_rcp_f32_e32 v1, v1
	v_rcp_f32_e32 v223, v223
	v_mul_f32_e32 v226, v224, v226
	v_mul_f32_e32 v202, v225, v202
	v_mul_f32_e32 v227, v1, v227
	v_mul_f32_e32 v203, v223, v203
	v_mul_f32_e32 v216, v226, v216
	v_mul_f32_e32 v217, v202, v217
	v_mul_f32_e32 v218, v227, v218
	v_mul_f32_e32 v219, v203, v219
	v_cvt_pk_bf16_f32 v226, v216, v217
	v_cvt_pk_bf16_f32 v227, v218, v219
	s_cmp_gt_i32 s14, 0xffff
	s_cbranch_scc1 .Lgc_skip_b_15
	s_lshr_b32 s17, s14, 2
	s_and_b32 s18, s14, 3
	s_lshl_b32 s17, s17, 12
	s_lshl_b32 s18, s18, 9
	s_add_i32 s17, s17, s18
	v_add_u32_e32 v225, s17, v6
	global_store_dwordx2 v225, v[226:227], s[24:25]
.Lgc_skip_b_15:
	s_mov_b32 s10, s19
	s_cmp_gt_i32 s10, 0xffff
	s_cbranch_scc0 .Lgc_loop
.Lgc_done:
	s_waitcnt vmcnt(0)
	s_nop 0
	s_nop 0
	s_nop 0
	s_nop 0
	s_nop 0
	s_nop 0
	s_nop 0
	s_nop 0
	s_nop 0
	s_nop 0
	s_nop 0
